# speedup vs baseline: 1.0615x; 1.0050x over previous
.LBB2_382:
	ds_read_b128 v[152:155], v151
	ds_read_b128 v[156:159], v151 offset:1024
	ds_read_b128 v[164:167], v151 offset:2048
	ds_read_b128 v[168:171], v151 offset:3072
	s_lshl_b32 s58, s84, 7
	s_add_u32 s59, s24, s58
	s_addc_u32 s91, s25, 0
	s_add_u32 s92, s59, 0x80
	s_addc_u32 s93, s91, 0
	s_add_i32 s56, s52, 0xc000
	s_mov_b32 m0, s56
	v_lshl_add_u64 v[160:161], s[92:93], 0, v[132:133]
	s_add_i32 s33, s52, 0xe000
	ds_read_b128 v[172:175], v147
	ds_read_b128 v[176:179], v147 offset:1024
	ds_read_b128 v[184:187], v146
	ds_read_b128 v[188:191], v146 offset:1024
	ds_read_b128 v[192:195], v145
	ds_read_b128 v[196:199], v145 offset:1024
	ds_read_b128 v[200:203], v144
	ds_read_b128 v[204:207], v144 offset:1024
	global_load_lds_dwordx4 v[160:161], off
	v_lshl_add_u64 v[160:161], s[92:93], 0, v[130:131]
	s_mov_b32 m0, s33
	s_nop 0
	global_load_lds_dwordx4 v[160:161], off
	s_waitcnt lgkmcnt(8)
	s_barrier
	s_setprio 1
	s_waitcnt lgkmcnt(0)
	v_mfma_f32_16x16x32_f16 v[126:129], v[152:155], v[172:175], v[126:129]
	v_mfma_f32_16x16x32_f16 v[122:125], v[164:167], v[172:175], v[122:125]
	v_mfma_f32_16x16x32_f16 v[118:121], v[152:155], v[184:187], v[118:121]
	v_mfma_f32_16x16x32_f16 v[114:117], v[164:167], v[184:187], v[114:117]
	v_mfma_f32_16x16x32_f16 v[110:113], v[152:155], v[192:195], v[110:113]
	v_mfma_f32_16x16x32_f16 v[106:109], v[164:167], v[192:195], v[106:109]
	v_mfma_f32_16x16x32_f16 v[102:105], v[152:155], v[200:203], v[102:105]
	v_mfma_f32_16x16x32_f16 v[98:101], v[164:167], v[200:203], v[98:101]
	v_mfma_f32_16x16x32_f16 v[126:129], v[156:159], v[176:179], v[126:129]
	v_mfma_f32_16x16x32_f16 v[122:125], v[168:171], v[176:179], v[122:125]
	v_mfma_f32_16x16x32_f16 v[118:121], v[156:159], v[188:191], v[118:121]
	v_mfma_f32_16x16x32_f16 v[114:117], v[168:171], v[188:191], v[114:117]
	v_mfma_f32_16x16x32_f16 v[110:113], v[156:159], v[196:199], v[110:113]
	v_mfma_f32_16x16x32_f16 v[106:109], v[168:171], v[196:199], v[106:109]
	v_mfma_f32_16x16x32_f16 v[102:105], v[156:159], v[204:207], v[102:105]
	v_mfma_f32_16x16x32_f16 v[98:101], v[168:171], v[204:207], v[98:101]
	s_setprio 0
	s_barrier
	s_add_i32 s57, s84, 2
	s_lshl_b32 s82, s57, 7
	s_add_u32 s92, s4, s82
	s_addc_u32 s93, s5, 0
	s_mov_b32 m0, s53
	v_lshl_add_u64 v[160:161], s[92:93], 0, v[162:163]
	s_add_u32 s92, s92, 0x40000
	s_addc_u32 s93, s93, 0
	ds_read_b128 v[208:211], v150
	ds_read_b128 v[212:215], v150 offset:1024
	ds_read_b128 v[216:219], v150 offset:2048
	ds_read_b128 v[220:223], v150 offset:3072
	global_load_lds_dwordx4 v[160:161], off
	s_mov_b32 m0, s55
	v_lshl_add_u64 v[160:161], s[92:93], 0, v[162:163]
	global_load_lds_dwordx4 v[160:161], off
	s_barrier
	s_setprio 1
	s_waitcnt lgkmcnt(0)
	v_mfma_f32_16x16x32_f16 v[94:97], v[208:211], v[172:175], v[94:97]
	v_mfma_f32_16x16x32_f16 v[90:93], v[216:219], v[172:175], v[90:93]
	v_mfma_f32_16x16x32_f16 v[86:89], v[208:211], v[184:187], v[86:89]
	v_mfma_f32_16x16x32_f16 v[82:85], v[216:219], v[184:187], v[82:85]
	v_mfma_f32_16x16x32_f16 v[78:81], v[208:211], v[192:195], v[78:81]
	v_mfma_f32_16x16x32_f16 v[74:77], v[216:219], v[192:195], v[74:77]
	v_mfma_f32_16x16x32_f16 v[70:73], v[208:211], v[200:203], v[70:73]
	v_mfma_f32_16x16x32_f16 v[66:69], v[216:219], v[200:203], v[66:69]
	v_mfma_f32_16x16x32_f16 v[94:97], v[212:215], v[176:179], v[94:97]
	v_mfma_f32_16x16x32_f16 v[90:93], v[220:223], v[176:179], v[90:93]
	v_mfma_f32_16x16x32_f16 v[86:89], v[212:215], v[188:191], v[86:89]
	v_mfma_f32_16x16x32_f16 v[82:85], v[220:223], v[188:191], v[82:85]
	v_mfma_f32_16x16x32_f16 v[78:81], v[212:215], v[196:199], v[78:81]
	v_mfma_f32_16x16x32_f16 v[74:77], v[220:223], v[196:199], v[74:77]
	v_mfma_f32_16x16x32_f16 v[70:73], v[212:215], v[204:207], v[70:73]
	v_mfma_f32_16x16x32_f16 v[66:69], v[220:223], v[204:207], v[66:69]
	s_setprio 0
	s_add_u32 s92, s24, s82
	s_addc_u32 s93, s25, 0
	s_mov_b32 m0, s52
	s_barrier
	v_lshl_add_u64 v[160:161], s[92:93], 0, v[134:135]
	ds_read_b128 v[172:175], v147 offset:16384
	ds_read_b128 v[176:179], v147 offset:17408
	ds_read_b128 v[184:187], v146 offset:16384
	ds_read_b128 v[188:191], v146 offset:17408
	ds_read_b128 v[192:195], v145 offset:16384
	ds_read_b128 v[196:199], v145 offset:17408
	ds_read_b128 v[200:203], v144 offset:16384
	ds_read_b128 v[204:207], v144 offset:17408
	global_load_lds_dwordx4 v[160:161], off
	v_lshl_add_u64 v[160:161], s[92:93], 0, v[136:137]
	s_mov_b32 m0, s86
	s_nop 0
	global_load_lds_dwordx4 v[160:161], off
	s_barrier
	s_setprio 1
	s_waitcnt lgkmcnt(0)
	v_mfma_f32_16x16x32_f16 v[62:65], v[152:155], v[172:175], v[62:65]
	v_mfma_f32_16x16x32_f16 v[58:61], v[164:167], v[172:175], v[58:61]
	v_mfma_f32_16x16x32_f16 v[54:57], v[152:155], v[184:187], v[54:57]
	v_mfma_f32_16x16x32_f16 v[50:53], v[164:167], v[184:187], v[50:53]
	v_mfma_f32_16x16x32_f16 v[46:49], v[152:155], v[192:195], v[46:49]
	v_mfma_f32_16x16x32_f16 v[42:45], v[164:167], v[192:195], v[42:45]
	v_mfma_f32_16x16x32_f16 v[38:41], v[152:155], v[200:203], v[38:41]
	v_mfma_f32_16x16x32_f16 v[34:37], v[164:167], v[200:203], v[34:37]
	v_mfma_f32_16x16x32_f16 v[62:65], v[156:159], v[176:179], v[62:65]
	v_mfma_f32_16x16x32_f16 v[58:61], v[168:171], v[176:179], v[58:61]
	v_mfma_f32_16x16x32_f16 v[54:57], v[156:159], v[188:191], v[54:57]
	v_mfma_f32_16x16x32_f16 v[50:53], v[168:171], v[188:191], v[50:53]
	v_mfma_f32_16x16x32_f16 v[46:49], v[156:159], v[196:199], v[46:49]
	v_mfma_f32_16x16x32_f16 v[42:45], v[168:171], v[196:199], v[42:45]
	v_mfma_f32_16x16x32_f16 v[38:41], v[156:159], v[204:207], v[38:41]
	v_mfma_f32_16x16x32_f16 v[34:37], v[168:171], v[204:207], v[34:37]
	s_setprio 0
	s_barrier
	s_add_u32 s94, s10, s82
	s_addc_u32 s95, s11, 0
	s_mov_b32 m0, s87
	v_lshl_add_u64 v[152:153], s[94:95], 0, v[162:163]
	s_add_u32 s94, s94, 0x40000
	s_addc_u32 s95, s95, 0
	global_load_lds_dwordx4 v[152:153], off
	s_mov_b32 m0, s88
	v_lshl_add_u64 v[152:153], s[94:95], 0, v[162:163]
	global_load_lds_dwordx4 v[152:153], off
	s_waitcnt vmcnt(6)
	s_barrier
	s_setprio 1
	v_mfma_f32_16x16x32_f16 v[30:33], v[208:211], v[172:175], v[30:33]
	v_mfma_f32_16x16x32_f16 v[26:29], v[216:219], v[172:175], v[26:29]
	v_mfma_f32_16x16x32_f16 v[22:25], v[208:211], v[184:187], v[22:25]
	v_mfma_f32_16x16x32_f16 v[18:21], v[216:219], v[184:187], v[18:21]
	v_mfma_f32_16x16x32_f16 v[14:17], v[208:211], v[192:195], v[14:17]
	v_mfma_f32_16x16x32_f16 v[10:13], v[216:219], v[192:195], v[10:13]
	v_mfma_f32_16x16x32_f16 v[6:9], v[208:211], v[200:203], v[6:9]
	v_mfma_f32_16x16x32_f16 v[2:5], v[216:219], v[200:203], v[2:5]
	v_mfma_f32_16x16x32_f16 v[30:33], v[212:215], v[176:179], v[30:33]
	v_mfma_f32_16x16x32_f16 v[26:29], v[220:223], v[176:179], v[26:29]
	v_mfma_f32_16x16x32_f16 v[22:25], v[212:215], v[188:191], v[22:25]
	v_mfma_f32_16x16x32_f16 v[18:21], v[220:223], v[188:191], v[18:21]
	v_mfma_f32_16x16x32_f16 v[14:17], v[212:215], v[196:199], v[14:17]
	v_mfma_f32_16x16x32_f16 v[10:13], v[220:223], v[196:199], v[10:13]
	v_mfma_f32_16x16x32_f16 v[6:9], v[212:215], v[204:207], v[6:9]
	v_mfma_f32_16x16x32_f16 v[2:5], v[220:223], v[204:207], v[2:5]
	s_setprio 0
	s_barrier
	ds_read_b128 v[152:155], v149
	ds_read_b128 v[156:159], v149 offset:1024
	ds_read_b128 v[164:167], v149 offset:2048
	ds_read_b128 v[168:171], v149 offset:3072
	s_mov_b32 m0, s89
	v_lshl_add_u64 v[160:161], s[92:93], 0, v[132:133]
	ds_read_b128 v[172:175], v147 offset:32768
	ds_read_b128 v[176:179], v147 offset:33792
	ds_read_b128 v[184:187], v146 offset:32768
	ds_read_b128 v[188:191], v146 offset:33792
	ds_read_b128 v[192:195], v145 offset:32768
	ds_read_b128 v[196:199], v145 offset:33792
	ds_read_b128 v[200:203], v144 offset:32768
	ds_read_b128 v[204:207], v144 offset:33792
	global_load_lds_dwordx4 v[160:161], off
	v_lshl_add_u64 v[160:161], s[92:93], 0, v[130:131]
	s_mov_b32 m0, s90
	s_nop 0
	global_load_lds_dwordx4 v[160:161], off
	s_waitcnt lgkmcnt(8)
	s_barrier
	s_setprio 1
	s_waitcnt lgkmcnt(0)
	v_mfma_f32_16x16x32_f16 v[126:129], v[152:155], v[172:175], v[126:129]
	v_mfma_f32_16x16x32_f16 v[122:125], v[164:167], v[172:175], v[122:125]
	v_mfma_f32_16x16x32_f16 v[118:121], v[152:155], v[184:187], v[118:121]
	v_mfma_f32_16x16x32_f16 v[114:117], v[164:167], v[184:187], v[114:117]
	v_mfma_f32_16x16x32_f16 v[110:113], v[152:155], v[192:195], v[110:113]
	v_mfma_f32_16x16x32_f16 v[106:109], v[164:167], v[192:195], v[106:109]
	v_mfma_f32_16x16x32_f16 v[102:105], v[152:155], v[200:203], v[102:105]
	v_mfma_f32_16x16x32_f16 v[98:101], v[164:167], v[200:203], v[98:101]
	v_mfma_f32_16x16x32_f16 v[126:129], v[156:159], v[176:179], v[126:129]
	v_mfma_f32_16x16x32_f16 v[122:125], v[168:171], v[176:179], v[122:125]
	v_mfma_f32_16x16x32_f16 v[118:121], v[156:159], v[188:191], v[118:121]
	v_mfma_f32_16x16x32_f16 v[114:117], v[168:171], v[188:191], v[114:117]
	v_mfma_f32_16x16x32_f16 v[110:113], v[156:159], v[196:199], v[110:113]
	v_mfma_f32_16x16x32_f16 v[106:109], v[168:171], v[196:199], v[106:109]
	v_mfma_f32_16x16x32_f16 v[102:105], v[156:159], v[204:207], v[102:105]
	v_mfma_f32_16x16x32_f16 v[98:101], v[168:171], v[204:207], v[98:101]
	s_setprio 0
	s_barrier
	s_add_u32 s82, s4, s58
	s_addc_u32 s83, s5, 0
	s_add_u32 s92, s82, 0x180
	s_addc_u32 s93, s83, 0
	s_add_i32 m0, s52, 0x18000
	v_lshl_add_u64 v[160:161], s[92:93], 0, v[162:163]
	s_add_u32 s92, s92, 0x40000
	s_addc_u32 s93, s93, 0
	ds_read_b128 v[208:211], v148
	ds_read_b128 v[212:215], v148 offset:1024
	ds_read_b128 v[216:219], v148 offset:2048
	ds_read_b128 v[220:223], v148 offset:3072
	global_load_lds_dwordx4 v[160:161], off
	s_add_i32 m0, s52, 0x1a000
	v_lshl_add_u64 v[160:161], s[92:93], 0, v[162:163]
	global_load_lds_dwordx4 v[160:161], off
	s_barrier
	s_setprio 1
	s_waitcnt lgkmcnt(0)
	v_mfma_f32_16x16x32_f16 v[94:97], v[208:211], v[172:175], v[94:97]
	v_mfma_f32_16x16x32_f16 v[90:93], v[216:219], v[172:175], v[90:93]
	v_mfma_f32_16x16x32_f16 v[86:89], v[208:211], v[184:187], v[86:89]
	v_mfma_f32_16x16x32_f16 v[82:85], v[216:219], v[184:187], v[82:85]
	v_mfma_f32_16x16x32_f16 v[78:81], v[208:211], v[192:195], v[78:81]
	v_mfma_f32_16x16x32_f16 v[74:77], v[216:219], v[192:195], v[74:77]
	v_mfma_f32_16x16x32_f16 v[70:73], v[208:211], v[200:203], v[70:73]
	v_mfma_f32_16x16x32_f16 v[66:69], v[216:219], v[200:203], v[66:69]
	v_mfma_f32_16x16x32_f16 v[94:97], v[212:215], v[176:179], v[94:97]
	v_mfma_f32_16x16x32_f16 v[90:93], v[220:223], v[176:179], v[90:93]
	v_mfma_f32_16x16x32_f16 v[86:89], v[212:215], v[188:191], v[86:89]
	v_mfma_f32_16x16x32_f16 v[82:85], v[220:223], v[188:191], v[82:85]
	v_mfma_f32_16x16x32_f16 v[78:81], v[212:215], v[196:199], v[78:81]
	v_mfma_f32_16x16x32_f16 v[74:77], v[220:223], v[196:199], v[74:77]
	v_mfma_f32_16x16x32_f16 v[70:73], v[212:215], v[204:207], v[70:73]
	v_mfma_f32_16x16x32_f16 v[66:69], v[220:223], v[204:207], v[66:69]
	s_setprio 0
	s_add_u32 s92, s59, 0x180
	s_addc_u32 s93, s91, 0
	s_mov_b32 m0, s34
	s_barrier
	v_lshl_add_u64 v[160:161], s[92:93], 0, v[134:135]
	ds_read_b128 v[172:175], v147 offset:49152
	ds_read_b128 v[176:179], v147 offset:50176
	ds_read_b128 v[184:187], v146 offset:49152
	ds_read_b128 v[188:191], v146 offset:50176
	ds_read_b128 v[192:195], v145 offset:49152
	ds_read_b128 v[196:199], v145 offset:50176
	ds_read_b128 v[200:203], v144 offset:49152
	ds_read_b128 v[204:207], v144 offset:50176
	global_load_lds_dwordx4 v[160:161], off
	v_lshl_add_u64 v[160:161], s[92:93], 0, v[136:137]
	s_mov_b32 m0, s35
	s_nop 0
	global_load_lds_dwordx4 v[160:161], off
	s_barrier
	s_setprio 1
	s_waitcnt lgkmcnt(0)
	v_mfma_f32_16x16x32_f16 v[62:65], v[152:155], v[172:175], v[62:65]
	v_mfma_f32_16x16x32_f16 v[58:61], v[164:167], v[172:175], v[58:61]
	v_mfma_f32_16x16x32_f16 v[54:57], v[152:155], v[184:187], v[54:57]
	v_mfma_f32_16x16x32_f16 v[50:53], v[164:167], v[184:187], v[50:53]
	v_mfma_f32_16x16x32_f16 v[46:49], v[152:155], v[192:195], v[46:49]
	v_mfma_f32_16x16x32_f16 v[42:45], v[164:167], v[192:195], v[42:45]
	v_mfma_f32_16x16x32_f16 v[38:41], v[152:155], v[200:203], v[38:41]
	v_mfma_f32_16x16x32_f16 v[34:37], v[164:167], v[200:203], v[34:37]
	v_mfma_f32_16x16x32_f16 v[62:65], v[156:159], v[176:179], v[62:65]
	v_mfma_f32_16x16x32_f16 v[58:61], v[168:171], v[176:179], v[58:61]
	v_mfma_f32_16x16x32_f16 v[54:57], v[156:159], v[188:191], v[54:57]
	v_mfma_f32_16x16x32_f16 v[50:53], v[168:171], v[188:191], v[50:53]
	v_mfma_f32_16x16x32_f16 v[46:49], v[156:159], v[196:199], v[46:49]
	v_mfma_f32_16x16x32_f16 v[42:45], v[168:171], v[196:199], v[42:45]
	v_mfma_f32_16x16x32_f16 v[38:41], v[156:159], v[204:207], v[38:41]
	v_mfma_f32_16x16x32_f16 v[34:37], v[168:171], v[204:207], v[34:37]
	s_setprio 0
	s_barrier
	s_add_u32 s58, s10, s58
	s_addc_u32 s59, s11, 0
	s_add_u32 s58, s58, 0x180
	s_addc_u32 s59, s59, 0
	s_add_i32 m0, s52, 0x1c000
	v_lshl_add_u64 v[152:153], s[58:59], 0, v[162:163]
	s_add_u32 s58, s58, 0x40000
	s_addc_u32 s59, s59, 0
	global_load_lds_dwordx4 v[152:153], off
	s_add_i32 m0, s52, 0x1e000
	v_lshl_add_u64 v[152:153], s[58:59], 0, v[162:163]
	global_load_lds_dwordx4 v[152:153], off
	s_waitcnt vmcnt(6)
	s_barrier
	s_setprio 1
	v_mfma_f32_16x16x32_f16 v[30:33], v[208:211], v[172:175], v[30:33]
	v_mfma_f32_16x16x32_f16 v[26:29], v[216:219], v[172:175], v[26:29]
	v_mfma_f32_16x16x32_f16 v[22:25], v[208:211], v[184:187], v[22:25]
	v_mfma_f32_16x16x32_f16 v[18:21], v[216:219], v[184:187], v[18:21]
	v_mfma_f32_16x16x32_f16 v[14:17], v[208:211], v[192:195], v[14:17]
	v_mfma_f32_16x16x32_f16 v[10:13], v[216:219], v[192:195], v[10:13]
	v_mfma_f32_16x16x32_f16 v[6:9], v[208:211], v[200:203], v[6:9]
	v_mfma_f32_16x16x32_f16 v[2:5], v[216:219], v[200:203], v[2:5]
	v_mfma_f32_16x16x32_f16 v[30:33], v[212:215], v[176:179], v[30:33]
	v_mfma_f32_16x16x32_f16 v[26:29], v[220:223], v[176:179], v[26:29]
	v_mfma_f32_16x16x32_f16 v[22:25], v[212:215], v[188:191], v[22:25]
	v_mfma_f32_16x16x32_f16 v[18:21], v[220:223], v[188:191], v[18:21]
	v_mfma_f32_16x16x32_f16 v[14:17], v[212:215], v[196:199], v[14:17]
	v_mfma_f32_16x16x32_f16 v[10:13], v[220:223], v[196:199], v[10:13]
	v_mfma_f32_16x16x32_f16 v[6:9], v[212:215], v[204:207], v[6:9]
	v_mfma_f32_16x16x32_f16 v[2:5], v[220:223], v[204:207], v[2:5]
	s_setprio 0
	s_cmp_lt_u32 s84, 28
	s_mov_b32 s84, s57
	s_barrier
	s_cbranch_scc1 .LBB2_382
	v_readlane_b32 s4, v244, 8
	v_readlane_b32 s5, v244, 9
	s_mov_b32 m0, s56
	ds_read_b128 v[134:137], v151
	ds_read_b128 v[152:155], v151 offset:1024
	ds_read_b128 v[156:159], v151 offset:2048
	ds_read_b128 v[164:167], v151 offset:3072
	ds_read_b128 v[168:171], v147
	ds_read_b128 v[172:175], v147 offset:1024
	ds_read_b128 v[176:179], v146
	ds_read_b128 v[184:187], v146 offset:1024
	ds_read_b128 v[188:191], v145
	ds_read_b128 v[192:195], v145 offset:1024
	ds_read_b128 v[196:199], v144
	ds_read_b128 v[200:203], v144 offset:1024
	v_lshl_add_u64 v[132:133], s[4:5], 0, v[132:133]
	global_load_lds_dwordx4 v[132:133], off
	v_lshl_add_u64 v[130:131], s[4:5], 0, v[130:131]
	s_mov_b32 m0, s33
	s_nop 0
	global_load_lds_dwordx4 v[130:131], off
	s_barrier
	s_setprio 1
	s_waitcnt lgkmcnt(0)
	v_mfma_f32_16x16x32_f16 v[126:129], v[134:137], v[168:171], v[126:129]
	v_mfma_f32_16x16x32_f16 v[122:125], v[156:159], v[168:171], v[122:125]
	v_mfma_f32_16x16x32_f16 v[110:113], v[134:137], v[188:191], v[110:113]
	v_mfma_f32_16x16x32_f16 v[106:109], v[156:159], v[188:191], v[106:109]
	v_mfma_f32_16x16x32_f16 v[126:129], v[152:155], v[172:175], v[126:129]
	v_mfma_f32_16x16x32_f16 v[122:125], v[164:167], v[172:175], v[122:125]
	v_mfma_f32_16x16x32_f16 v[118:121], v[134:137], v[176:179], v[118:121]
	v_mfma_f32_16x16x32_f16 v[114:117], v[156:159], v[176:179], v[114:117]
	v_mfma_f32_16x16x32_f16 v[110:113], v[152:155], v[192:195], v[110:113]
	v_mfma_f32_16x16x32_f16 v[106:109], v[164:167], v[192:195], v[106:109]
	v_mfma_f32_16x16x32_f16 v[102:105], v[134:137], v[196:199], v[102:105]
	v_mfma_f32_16x16x32_f16 v[98:101], v[156:159], v[196:199], v[98:101]
	v_mfma_f32_16x16x32_f16 v[130:133], v[152:155], v[184:187], v[118:121]
	v_mfma_f32_16x16x32_f16 v[204:207], v[164:167], v[184:187], v[114:117]
	v_mfma_f32_16x16x32_f16 v[208:211], v[152:155], v[200:203], v[102:105]
	v_mfma_f32_16x16x32_f16 v[212:215], v[164:167], v[200:203], v[98:101]
	s_setprio 0
	s_barrier
	s_nop 1
	ds_read_b128 v[98:101], v150
	ds_read_b128 v[102:105], v150 offset:1024
	ds_read_b128 v[114:117], v150 offset:2048
	ds_read_b128 v[118:121], v150 offset:3072
	s_barrier
	s_setprio 1
	s_waitcnt lgkmcnt(0)
	v_mfma_f32_16x16x32_f16 v[94:97], v[98:101], v[168:171], v[94:97]
	v_mfma_f32_16x16x32_f16 v[90:93], v[114:117], v[168:171], v[90:93]
	v_mfma_f32_16x16x32_f16 v[78:81], v[98:101], v[188:191], v[78:81]
	v_mfma_f32_16x16x32_f16 v[74:77], v[114:117], v[188:191], v[74:77]
	v_mfma_f32_16x16x32_f16 v[94:97], v[102:105], v[172:175], v[94:97]
	v_mfma_f32_16x16x32_f16 v[90:93], v[118:121], v[172:175], v[90:93]
	v_mfma_f32_16x16x32_f16 v[86:89], v[98:101], v[176:179], v[86:89]
	v_mfma_f32_16x16x32_f16 v[82:85], v[114:117], v[176:179], v[82:85]
	v_mfma_f32_16x16x32_f16 v[78:81], v[102:105], v[192:195], v[78:81]
	v_mfma_f32_16x16x32_f16 v[74:77], v[118:121], v[192:195], v[74:77]
	v_mfma_f32_16x16x32_f16 v[70:73], v[98:101], v[196:199], v[70:73]
	v_mfma_f32_16x16x32_f16 v[66:69], v[114:117], v[196:199], v[66:69]
	v_mfma_f32_16x16x32_f16 v[168:171], v[102:105], v[184:187], v[86:89]
	v_mfma_f32_16x16x32_f16 v[172:175], v[118:121], v[184:187], v[82:85]
	v_mfma_f32_16x16x32_f16 v[176:179], v[102:105], v[200:203], v[70:73]
	v_mfma_f32_16x16x32_f16 v[184:187], v[118:121], v[200:203], v[66:69]
	s_setprio 0
	s_barrier
	s_nop 1
	ds_read_b128 v[66:69], v147 offset:16384
	ds_read_b128 v[70:73], v147 offset:17408
	ds_read_b128 v[82:85], v146 offset:16384
	ds_read_b128 v[86:89], v146 offset:17408
	ds_read_b128 v[188:191], v145 offset:16384
	ds_read_b128 v[192:195], v145 offset:17408
	ds_read_b128 v[196:199], v144 offset:16384
	ds_read_b128 v[200:203], v144 offset:17408
	s_waitcnt vmcnt(4)
	s_barrier
	s_setprio 1
	s_waitcnt lgkmcnt(0)
	v_mfma_f32_16x16x32_f16 v[62:65], v[134:137], v[66:69], v[62:65]
	v_mfma_f32_16x16x32_f16 v[58:61], v[156:159], v[66:69], v[58:61]
	v_mfma_f32_16x16x32_f16 v[46:49], v[134:137], v[188:191], v[46:49]
	v_mfma_f32_16x16x32_f16 v[42:45], v[156:159], v[188:191], v[42:45]
	v_mfma_f32_16x16x32_f16 v[62:65], v[152:155], v[70:73], v[62:65]
	v_mfma_f32_16x16x32_f16 v[58:61], v[164:167], v[70:73], v[58:61]
	v_mfma_f32_16x16x32_f16 v[54:57], v[134:137], v[82:85], v[54:57]
	v_mfma_f32_16x16x32_f16 v[50:53], v[156:159], v[82:85], v[50:53]
	v_mfma_f32_16x16x32_f16 v[46:49], v[152:155], v[192:195], v[46:49]
	v_mfma_f32_16x16x32_f16 v[42:45], v[164:167], v[192:195], v[42:45]
	v_mfma_f32_16x16x32_f16 v[38:41], v[134:137], v[196:199], v[38:41]
	v_mfma_f32_16x16x32_f16 v[34:37], v[156:159], v[196:199], v[34:37]
	v_mfma_f32_16x16x32_f16 v[216:219], v[152:155], v[86:89], v[54:57]
	v_mfma_f32_16x16x32_f16 v[220:223], v[164:167], v[86:89], v[50:53]
	v_mfma_f32_16x16x32_f16 v[134:137], v[152:155], v[200:203], v[38:41]
	v_mfma_f32_16x16x32_f16 v[150:153], v[164:167], v[200:203], v[34:37]
	s_setprio 0
	s_setprio 1
	v_mfma_f32_16x16x32_f16 v[30:33], v[98:101], v[66:69], v[30:33]
	v_mfma_f32_16x16x32_f16 v[26:29], v[114:117], v[66:69], v[26:29]
	v_mfma_f32_16x16x32_f16 v[14:17], v[98:101], v[188:191], v[14:17]
	v_mfma_f32_16x16x32_f16 v[10:13], v[114:117], v[188:191], v[10:13]
	v_mfma_f32_16x16x32_f16 v[30:33], v[102:105], v[70:73], v[30:33]
	v_mfma_f32_16x16x32_f16 v[26:29], v[118:121], v[70:73], v[26:29]
	v_mfma_f32_16x16x32_f16 v[22:25], v[98:101], v[82:85], v[22:25]
	v_mfma_f32_16x16x32_f16 v[18:21], v[114:117], v[82:85], v[18:21]
	v_mfma_f32_16x16x32_f16 v[14:17], v[102:105], v[192:195], v[14:17]
	v_mfma_f32_16x16x32_f16 v[10:13], v[118:121], v[192:195], v[10:13]
	v_mfma_f32_16x16x32_f16 v[6:9], v[98:101], v[196:199], v[6:9]
	v_mfma_f32_16x16x32_f16 v[2:5], v[114:117], v[196:199], v[2:5]
	v_mfma_f32_16x16x32_f16 v[154:157], v[102:105], v[86:89], v[22:25]
	v_mfma_f32_16x16x32_f16 v[158:161], v[118:121], v[86:89], v[18:21]
	v_mfma_f32_16x16x32_f16 v[164:167], v[102:105], v[200:203], v[6:9]
	v_mfma_f32_16x16x32_f16 v[188:191], v[118:121], v[200:203], v[2:5]
	s_setprio 0
	s_barrier
	s_nop 1
	ds_read_b128 v[2:5], v149
	ds_read_b128 v[6:9], v149 offset:1024
	ds_read_b128 v[192:195], v149 offset:2048
	ds_read_b128 v[196:199], v149 offset:3072
	ds_read_b128 v[18:21], v147 offset:32768
	ds_read_b128 v[22:25], v147 offset:33792
	ds_read_b128 v[34:37], v146 offset:32768
	ds_read_b128 v[38:41], v146 offset:33792
	ds_read_b128 v[50:53], v145 offset:32768
	ds_read_b128 v[54:57], v145 offset:33792
	ds_read_b128 v[200:203], v144 offset:32768
	ds_read_b128 v[224:227], v144 offset:33792
	s_waitcnt vmcnt(2)
	s_barrier
	s_setprio 1
	s_waitcnt lgkmcnt(0)
	v_mfma_f32_16x16x32_f16 v[66:69], v[2:5], v[18:21], v[126:129]
	v_mfma_f32_16x16x32_f16 v[118:121], v[6:9], v[22:25], v[66:69]
	v_mfma_f32_16x16x32_f16 v[66:69], v[192:195], v[18:21], v[122:125]
	v_mfma_f32_16x16x32_f16 v[114:117], v[196:199], v[22:25], v[66:69]
	v_mfma_f32_16x16x32_f16 v[66:69], v[2:5], v[34:37], v[130:133]
	v_mfma_f32_16x16x32_f16 v[102:105], v[6:9], v[38:41], v[66:69]
	v_mfma_f32_16x16x32_f16 v[66:69], v[192:195], v[34:37], v[204:207]
	v_mfma_f32_16x16x32_f16 v[98:101], v[196:199], v[38:41], v[66:69]
	v_mfma_f32_16x16x32_f16 v[66:69], v[2:5], v[50:53], v[110:113]
	v_mfma_f32_16x16x32_f16 v[86:89], v[6:9], v[54:57], v[66:69]
	v_mfma_f32_16x16x32_f16 v[66:69], v[192:195], v[50:53], v[106:109]
	v_mfma_f32_16x16x32_f16 v[82:85], v[196:199], v[54:57], v[66:69]
	v_mfma_f32_16x16x32_f16 v[66:69], v[2:5], v[200:203], v[208:211]
	v_mfma_f32_16x16x32_f16 v[70:73], v[6:9], v[224:227], v[66:69]
	v_mfma_f32_16x16x32_f16 v[66:69], v[192:195], v[200:203], v[212:215]
	v_mfma_f32_16x16x32_f16 v[66:69], v[196:199], v[224:227], v[66:69]
	s_setprio 0
	s_barrier
	ds_read_b128 v[130:133], v148
	ds_read_b128 v[204:207], v148 offset:1024
	ds_read_b128 v[208:211], v148 offset:2048
	ds_read_b128 v[212:215], v148 offset:3072
	s_waitcnt vmcnt(0)
	s_barrier
	s_setprio 1
	s_waitcnt lgkmcnt(0)
	v_mfma_f32_16x16x32_f16 v[94:97], v[130:133], v[18:21], v[94:97]
	v_mfma_f32_16x16x32_f16 v[18:21], v[208:211], v[18:21], v[90:93]
	v_mfma_f32_16x16x32_f16 v[122:125], v[212:215], v[22:25], v[18:21]
	v_mfma_f32_16x16x32_f16 v[18:21], v[130:133], v[34:37], v[168:171]
	v_mfma_f32_16x16x32_f16 v[110:113], v[204:207], v[38:41], v[18:21]
	v_mfma_f32_16x16x32_f16 v[18:21], v[208:211], v[34:37], v[172:175]
	v_mfma_f32_16x16x32_f16 v[106:109], v[212:215], v[38:41], v[18:21]
	v_mfma_f32_16x16x32_f16 v[18:21], v[130:133], v[50:53], v[78:81]
	v_mfma_f32_16x16x32_f16 v[126:129], v[204:207], v[22:25], v[94:97]
	v_mfma_f32_16x16x32_f16 v[94:97], v[204:207], v[54:57], v[18:21]
	v_mfma_f32_16x16x32_f16 v[18:21], v[208:211], v[50:53], v[74:77]
	v_mfma_f32_16x16x32_f16 v[90:93], v[212:215], v[54:57], v[18:21]
	v_mfma_f32_16x16x32_f16 v[18:21], v[130:133], v[200:203], v[176:179]
	v_mfma_f32_16x16x32_f16 v[78:81], v[204:207], v[224:227], v[18:21]
	v_mfma_f32_16x16x32_f16 v[18:21], v[208:211], v[200:203], v[184:187]
	v_mfma_f32_16x16x32_f16 v[74:77], v[212:215], v[224:227], v[18:21]
	s_setprio 0
	s_barrier
	ds_read_b128 v[168:171], v147 offset:49152
	ds_read_b128 v[172:175], v147 offset:50176
	ds_read_b128 v[176:179], v146 offset:49152
	ds_read_b128 v[146:149], v146 offset:50176
	ds_read_b128 v[184:187], v145 offset:49152
	ds_read_b128 v[200:203], v145 offset:50176
	ds_read_b128 v[224:227], v144 offset:49152
	ds_read_b128 v[228:231], v144 offset:50176
	s_barrier
	s_setprio 1
	s_waitcnt lgkmcnt(0)
	v_mfma_f32_16x16x32_f16 v[18:21], v[2:5], v[168:171], v[62:65]
	v_mfma_f32_16x16x32_f16 v[54:57], v[6:9], v[172:175], v[18:21]
	v_mfma_f32_16x16x32_f16 v[18:21], v[192:195], v[168:171], v[58:61]
	v_mfma_f32_16x16x32_f16 v[50:53], v[196:199], v[172:175], v[18:21]
	v_mfma_f32_16x16x32_f16 v[18:21], v[2:5], v[176:179], v[216:219]
	v_mfma_f32_16x16x32_f16 v[38:41], v[6:9], v[146:149], v[18:21]
	v_mfma_f32_16x16x32_f16 v[18:21], v[192:195], v[176:179], v[220:223]
	v_mfma_f32_16x16x32_f16 v[34:37], v[196:199], v[146:149], v[18:21]
	v_mfma_f32_16x16x32_f16 v[18:21], v[2:5], v[184:187], v[46:49]
	v_mfma_f32_16x16x32_f16 v[2:5], v[2:5], v[224:227], v[134:137]
	v_mfma_f32_16x16x32_f16 v[22:25], v[6:9], v[200:203], v[18:21]
	v_mfma_f32_16x16x32_f16 v[18:21], v[192:195], v[184:187], v[42:45]
	v_mfma_f32_16x16x32_f16 v[6:9], v[6:9], v[228:231], v[2:5]
	v_mfma_f32_16x16x32_f16 v[2:5], v[192:195], v[224:227], v[150:153]
	v_mfma_f32_16x16x32_f16 v[18:21], v[196:199], v[200:203], v[18:21]
	v_mfma_f32_16x16x32_f16 v[2:5], v[196:199], v[228:231], v[2:5]
	s_setprio 0
	s_setprio 1
	v_mfma_f32_16x16x32_f16 v[26:29], v[208:211], v[168:171], v[26:29]
	v_mfma_f32_16x16x32_f16 v[58:61], v[212:215], v[172:175], v[26:29]
	v_mfma_f32_16x16x32_f16 v[26:29], v[130:133], v[176:179], v[154:157]
	v_mfma_f32_16x16x32_f16 v[46:49], v[204:207], v[146:149], v[26:29]
	v_mfma_f32_16x16x32_f16 v[26:29], v[208:211], v[176:179], v[158:161]
	v_mfma_f32_16x16x32_f16 v[10:13], v[208:211], v[184:187], v[10:13]
	v_mfma_f32_16x16x32_f16 v[30:33], v[130:133], v[168:171], v[30:33]
	v_mfma_f32_16x16x32_f16 v[42:45], v[212:215], v[146:149], v[26:29]
	v_mfma_f32_16x16x32_f16 v[14:17], v[130:133], v[184:187], v[14:17]
	v_mfma_f32_16x16x32_f16 v[26:29], v[212:215], v[200:203], v[10:13]
	v_mfma_f32_16x16x32_f16 v[10:13], v[130:133], v[224:227], v[164:167]
	v_mfma_f32_16x16x32_f16 v[62:65], v[204:207], v[172:175], v[30:33]
	v_mfma_f32_16x16x32_f16 v[30:33], v[204:207], v[200:203], v[14:17]
	v_mfma_f32_16x16x32_f16 v[14:17], v[204:207], v[228:231], v[10:13]
	v_mfma_f32_16x16x32_f16 v[10:13], v[208:211], v[224:227], v[188:191]
	v_mfma_f32_16x16x32_f16 v[10:13], v[212:215], v[228:231], v[10:13]
	s_setprio 0

.LBB2_385:
	s_or_b64 exec, exec, s[4:5]
	v_and_b32_e32 v170, 63, v141
	v_add_u32_e32 v171, v143, v139
	v_mul_u32_u24_e32 v160, 0x110, v171
	v_lshlrev_b32_e32 v172, 6, v142
	v_lshl_add_u32 v172, v140, 3, v172
	v_add_u32_e32 v160, v160, v172
	v_lshrrev_b32_e32 v173, 4, v170
	v_lshl_add_u32 v173, v138, 5, v173
	v_and_b32_e32 v174, 15, v170
	v_mul_u32_u24_e32 v161, 0x110, v173
	v_lshl_add_u32 v161, v174, 4, v161
	s_lshl_b32 s4, s96, 19
	s_lshl_b32 s5, s54, 8
	s_add_u32 s4, s4, s5
	v_lshl_add_u32 v164, v173, 11, s4
	v_lshl_add_u32 v164, v174, 4, v164
	v_mul_f32_e32 v144, v118, v126
	v_mul_f32_e32 v145, v119, v127
	v_mul_f32_e32 v146, v120, v128
	v_mul_f32_e32 v147, v121, v129
	v_mul_f32_e32 v148, 0xbfb8aa3b, v118
	v_mul_f32_e32 v149, 0xbfb8aa3b, v119
	v_mul_f32_e32 v150, 0xbfb8aa3b, v120
	v_mul_f32_e32 v151, 0xbfb8aa3b, v121
	v_exp_f32_e32 v148, v148
	v_exp_f32_e32 v149, v149
	v_exp_f32_e32 v150, v150
	v_exp_f32_e32 v151, v151
	v_add_f32_e32 v148, 1.0, v148
	v_add_f32_e32 v149, 1.0, v149
	v_add_f32_e32 v150, 1.0, v150
	v_add_f32_e32 v151, 1.0, v151
	v_rcp_f32_e32 v148, v148
	v_rcp_f32_e32 v149, v149
	v_rcp_f32_e32 v150, v150
	v_rcp_f32_e32 v151, v151
	v_mul_f32_e32 v144, v148, v144
	v_mul_f32_e32 v145, v149, v145
	v_mul_f32_e32 v146, v150, v146
	v_mul_f32_e32 v147, v151, v147
	v_cvt_pk_f16_f32 v152, v144, v145
	v_cvt_pk_f16_f32 v153, v146, v147
	ds_write_b64 v160, v[152:153]
	v_mul_f32_e32 v144, v114, v122
	v_mul_f32_e32 v145, v115, v123
	v_mul_f32_e32 v146, v116, v124
	v_mul_f32_e32 v147, v117, v125
	v_mul_f32_e32 v148, 0xbfb8aa3b, v114
	v_mul_f32_e32 v149, 0xbfb8aa3b, v115
	v_mul_f32_e32 v150, 0xbfb8aa3b, v116
	v_mul_f32_e32 v151, 0xbfb8aa3b, v117
	v_exp_f32_e32 v148, v148
	v_exp_f32_e32 v149, v149
	v_exp_f32_e32 v150, v150
	v_exp_f32_e32 v151, v151
	v_add_f32_e32 v148, 1.0, v148
	v_add_f32_e32 v149, 1.0, v149
	v_add_f32_e32 v150, 1.0, v150
	v_add_f32_e32 v151, 1.0, v151
	v_rcp_f32_e32 v148, v148
	v_rcp_f32_e32 v149, v149
	v_rcp_f32_e32 v150, v150
	v_rcp_f32_e32 v151, v151
	v_mul_f32_e32 v144, v148, v144
	v_mul_f32_e32 v145, v149, v145
	v_mul_f32_e32 v146, v150, v146
	v_mul_f32_e32 v147, v151, v147
	v_cvt_pk_f16_f32 v154, v144, v145
	v_cvt_pk_f16_f32 v155, v146, v147
	ds_write_b64 v160, v[154:155] offset:32
	v_mul_f32_e32 v144, v102, v110
	v_mul_f32_e32 v145, v103, v111
	v_mul_f32_e32 v146, v104, v112
	v_mul_f32_e32 v147, v105, v113
	v_mul_f32_e32 v148, 0xbfb8aa3b, v102
	v_mul_f32_e32 v149, 0xbfb8aa3b, v103
	v_mul_f32_e32 v150, 0xbfb8aa3b, v104
	v_mul_f32_e32 v151, 0xbfb8aa3b, v105
	v_exp_f32_e32 v148, v148
	v_exp_f32_e32 v149, v149
	v_exp_f32_e32 v150, v150
	v_exp_f32_e32 v151, v151
	v_add_f32_e32 v148, 1.0, v148
	v_add_f32_e32 v149, 1.0, v149
	v_add_f32_e32 v150, 1.0, v150
	v_add_f32_e32 v151, 1.0, v151
	v_rcp_f32_e32 v148, v148
	v_rcp_f32_e32 v149, v149
	v_rcp_f32_e32 v150, v150
	v_rcp_f32_e32 v151, v151
	v_mul_f32_e32 v144, v148, v144
	v_mul_f32_e32 v145, v149, v145
	v_mul_f32_e32 v146, v150, v146
	v_mul_f32_e32 v147, v151, v147
	v_cvt_pk_f16_f32 v156, v144, v145
	v_cvt_pk_f16_f32 v157, v146, v147
	ds_write_b64 v160, v[156:157] offset:4352
	v_mul_f32_e32 v144, v98, v106
	v_mul_f32_e32 v145, v99, v107
	v_mul_f32_e32 v146, v100, v108
	v_mul_f32_e32 v147, v101, v109
	v_mul_f32_e32 v148, 0xbfb8aa3b, v98
	v_mul_f32_e32 v149, 0xbfb8aa3b, v99
	v_mul_f32_e32 v150, 0xbfb8aa3b, v100
	v_mul_f32_e32 v151, 0xbfb8aa3b, v101
	v_exp_f32_e32 v148, v148
	v_exp_f32_e32 v149, v149
	v_exp_f32_e32 v150, v150
	v_exp_f32_e32 v151, v151
	v_add_f32_e32 v148, 1.0, v148
	v_add_f32_e32 v149, 1.0, v149
	v_add_f32_e32 v150, 1.0, v150
	v_add_f32_e32 v151, 1.0, v151
	v_rcp_f32_e32 v148, v148
	v_rcp_f32_e32 v149, v149
	v_rcp_f32_e32 v150, v150
	v_rcp_f32_e32 v151, v151
	v_mul_f32_e32 v144, v148, v144
	v_mul_f32_e32 v145, v149, v145
	v_mul_f32_e32 v146, v150, v146
	v_mul_f32_e32 v147, v151, v147
	v_cvt_pk_f16_f32 v158, v144, v145
	v_cvt_pk_f16_f32 v159, v146, v147
	ds_write_b64 v160, v[158:159] offset:4384
	v_mul_f32_e32 v144, v86, v94
	v_mul_f32_e32 v145, v87, v95
	v_mul_f32_e32 v146, v88, v96
	v_mul_f32_e32 v147, v89, v97
	v_mul_f32_e32 v148, 0xbfb8aa3b, v86
	v_mul_f32_e32 v149, 0xbfb8aa3b, v87
	v_mul_f32_e32 v150, 0xbfb8aa3b, v88
	v_mul_f32_e32 v151, 0xbfb8aa3b, v89
	v_exp_f32_e32 v148, v148
	v_exp_f32_e32 v149, v149
	v_exp_f32_e32 v150, v150
	v_exp_f32_e32 v151, v151
	v_add_f32_e32 v148, 1.0, v148
	v_add_f32_e32 v149, 1.0, v149
	v_add_f32_e32 v150, 1.0, v150
	v_add_f32_e32 v151, 1.0, v151
	v_rcp_f32_e32 v148, v148
	v_rcp_f32_e32 v149, v149
	v_rcp_f32_e32 v150, v150
	v_rcp_f32_e32 v151, v151
	v_mul_f32_e32 v144, v148, v144
	v_mul_f32_e32 v145, v149, v145
	v_mul_f32_e32 v146, v150, v146
	v_mul_f32_e32 v147, v151, v147
	v_cvt_pk_f16_f32 v152, v144, v145
	v_cvt_pk_f16_f32 v153, v146, v147
	ds_write_b64 v160, v[152:153] offset:8704
	v_mul_f32_e32 v144, v82, v90
	v_mul_f32_e32 v145, v83, v91
	v_mul_f32_e32 v146, v84, v92
	v_mul_f32_e32 v147, v85, v93
	v_mul_f32_e32 v148, 0xbfb8aa3b, v82
	v_mul_f32_e32 v149, 0xbfb8aa3b, v83
	v_mul_f32_e32 v150, 0xbfb8aa3b, v84
	v_mul_f32_e32 v151, 0xbfb8aa3b, v85
	v_exp_f32_e32 v148, v148
	v_exp_f32_e32 v149, v149
	v_exp_f32_e32 v150, v150
	v_exp_f32_e32 v151, v151
	v_add_f32_e32 v148, 1.0, v148
	v_add_f32_e32 v149, 1.0, v149
	v_add_f32_e32 v150, 1.0, v150
	v_add_f32_e32 v151, 1.0, v151
	v_rcp_f32_e32 v148, v148
	v_rcp_f32_e32 v149, v149
	v_rcp_f32_e32 v150, v150
	v_rcp_f32_e32 v151, v151
	v_mul_f32_e32 v144, v148, v144
	v_mul_f32_e32 v145, v149, v145
	v_mul_f32_e32 v146, v150, v146
	v_mul_f32_e32 v147, v151, v147
	v_cvt_pk_f16_f32 v154, v144, v145
	v_cvt_pk_f16_f32 v155, v146, v147
	ds_write_b64 v160, v[154:155] offset:8736
	v_mul_f32_e32 v144, v70, v78
	v_mul_f32_e32 v145, v71, v79
	v_mul_f32_e32 v146, v72, v80
	v_mul_f32_e32 v147, v73, v81
	v_mul_f32_e32 v148, 0xbfb8aa3b, v70
	v_mul_f32_e32 v149, 0xbfb8aa3b, v71
	v_mul_f32_e32 v150, 0xbfb8aa3b, v72
	v_mul_f32_e32 v151, 0xbfb8aa3b, v73
	v_exp_f32_e32 v148, v148
	v_exp_f32_e32 v149, v149
	v_exp_f32_e32 v150, v150
	v_exp_f32_e32 v151, v151
	v_add_f32_e32 v148, 1.0, v148
	v_add_f32_e32 v149, 1.0, v149
	v_add_f32_e32 v150, 1.0, v150
	v_add_f32_e32 v151, 1.0, v151
	v_rcp_f32_e32 v148, v148
	v_rcp_f32_e32 v149, v149
	v_rcp_f32_e32 v150, v150
	v_rcp_f32_e32 v151, v151
	v_mul_f32_e32 v144, v148, v144
	v_mul_f32_e32 v145, v149, v145
	v_mul_f32_e32 v146, v150, v146
	v_mul_f32_e32 v147, v151, v147
	v_cvt_pk_f16_f32 v156, v144, v145
	v_cvt_pk_f16_f32 v157, v146, v147
	ds_write_b64 v160, v[156:157] offset:13056
	v_mul_f32_e32 v144, v66, v74
	v_mul_f32_e32 v145, v67, v75
	v_mul_f32_e32 v146, v68, v76
	v_mul_f32_e32 v147, v69, v77
	v_mul_f32_e32 v148, 0xbfb8aa3b, v66
	v_mul_f32_e32 v149, 0xbfb8aa3b, v67
	v_mul_f32_e32 v150, 0xbfb8aa3b, v68
	v_mul_f32_e32 v151, 0xbfb8aa3b, v69
	v_exp_f32_e32 v148, v148
	v_exp_f32_e32 v149, v149
	v_exp_f32_e32 v150, v150
	v_exp_f32_e32 v151, v151
	v_add_f32_e32 v148, 1.0, v148
	v_add_f32_e32 v149, 1.0, v149
	v_add_f32_e32 v150, 1.0, v150
	v_add_f32_e32 v151, 1.0, v151
	v_rcp_f32_e32 v148, v148
	v_rcp_f32_e32 v149, v149
	v_rcp_f32_e32 v150, v150
	v_rcp_f32_e32 v151, v151
	v_mul_f32_e32 v144, v148, v144
	v_mul_f32_e32 v145, v149, v145
	v_mul_f32_e32 v146, v150, v146
	v_mul_f32_e32 v147, v151, v147
	v_cvt_pk_f16_f32 v158, v144, v145
	v_cvt_pk_f16_f32 v159, v146, v147
	ds_write_b64 v160, v[158:159] offset:13088
	v_mul_f32_e32 v144, v54, v62
	v_mul_f32_e32 v145, v55, v63
	v_mul_f32_e32 v146, v56, v64
	v_mul_f32_e32 v147, v57, v65
	v_mul_f32_e32 v148, 0xbfb8aa3b, v54
	v_mul_f32_e32 v149, 0xbfb8aa3b, v55
	v_mul_f32_e32 v150, 0xbfb8aa3b, v56
	v_mul_f32_e32 v151, 0xbfb8aa3b, v57
	v_exp_f32_e32 v148, v148
	v_exp_f32_e32 v149, v149
	v_exp_f32_e32 v150, v150
	v_exp_f32_e32 v151, v151
	v_add_f32_e32 v148, 1.0, v148
	v_add_f32_e32 v149, 1.0, v149
	v_add_f32_e32 v150, 1.0, v150
	v_add_f32_e32 v151, 1.0, v151
	v_rcp_f32_e32 v148, v148
	v_rcp_f32_e32 v149, v149
	v_rcp_f32_e32 v150, v150
	v_rcp_f32_e32 v151, v151
	v_mul_f32_e32 v144, v148, v144
	v_mul_f32_e32 v145, v149, v145
	v_mul_f32_e32 v146, v150, v146
	v_mul_f32_e32 v147, v151, v147
	v_cvt_pk_f16_f32 v152, v144, v145
	v_cvt_pk_f16_f32 v153, v146, v147
	ds_write_b64 v160, v[152:153] offset:34816
	v_mul_f32_e32 v144, v50, v58
	v_mul_f32_e32 v145, v51, v59
	v_mul_f32_e32 v146, v52, v60
	v_mul_f32_e32 v147, v53, v61
	v_mul_f32_e32 v148, 0xbfb8aa3b, v50
	v_mul_f32_e32 v149, 0xbfb8aa3b, v51
	v_mul_f32_e32 v150, 0xbfb8aa3b, v52
	v_mul_f32_e32 v151, 0xbfb8aa3b, v53
	v_exp_f32_e32 v148, v148
	v_exp_f32_e32 v149, v149
	v_exp_f32_e32 v150, v150
	v_exp_f32_e32 v151, v151
	v_add_f32_e32 v148, 1.0, v148
	v_add_f32_e32 v149, 1.0, v149
	v_add_f32_e32 v150, 1.0, v150
	v_add_f32_e32 v151, 1.0, v151
	v_rcp_f32_e32 v148, v148
	v_rcp_f32_e32 v149, v149
	v_rcp_f32_e32 v150, v150
	v_rcp_f32_e32 v151, v151
	v_mul_f32_e32 v144, v148, v144
	v_mul_f32_e32 v145, v149, v145
	v_mul_f32_e32 v146, v150, v146
	v_mul_f32_e32 v147, v151, v147
	v_cvt_pk_f16_f32 v154, v144, v145
	v_cvt_pk_f16_f32 v155, v146, v147
	ds_write_b64 v160, v[154:155] offset:34848
	v_mul_f32_e32 v144, v38, v46
	v_mul_f32_e32 v145, v39, v47
	v_mul_f32_e32 v146, v40, v48
	v_mul_f32_e32 v147, v41, v49
	v_mul_f32_e32 v148, 0xbfb8aa3b, v38
	v_mul_f32_e32 v149, 0xbfb8aa3b, v39
	v_mul_f32_e32 v150, 0xbfb8aa3b, v40
	v_mul_f32_e32 v151, 0xbfb8aa3b, v41
	v_exp_f32_e32 v148, v148
	v_exp_f32_e32 v149, v149
	v_exp_f32_e32 v150, v150
	v_exp_f32_e32 v151, v151
	v_add_f32_e32 v148, 1.0, v148
	v_add_f32_e32 v149, 1.0, v149
	v_add_f32_e32 v150, 1.0, v150
	v_add_f32_e32 v151, 1.0, v151
	v_rcp_f32_e32 v148, v148
	v_rcp_f32_e32 v149, v149
	v_rcp_f32_e32 v150, v150
	v_rcp_f32_e32 v151, v151
	v_mul_f32_e32 v144, v148, v144
	v_mul_f32_e32 v145, v149, v145
	v_mul_f32_e32 v146, v150, v146
	v_mul_f32_e32 v147, v151, v147
	v_cvt_pk_f16_f32 v156, v144, v145
	v_cvt_pk_f16_f32 v157, v146, v147
	ds_write_b64 v160, v[156:157] offset:39168
	v_mul_f32_e32 v144, v34, v42
	v_mul_f32_e32 v145, v35, v43
	v_mul_f32_e32 v146, v36, v44
	v_mul_f32_e32 v147, v37, v45
	v_mul_f32_e32 v148, 0xbfb8aa3b, v34
	v_mul_f32_e32 v149, 0xbfb8aa3b, v35
	v_mul_f32_e32 v150, 0xbfb8aa3b, v36
	v_mul_f32_e32 v151, 0xbfb8aa3b, v37
	v_exp_f32_e32 v148, v148
	v_exp_f32_e32 v149, v149
	v_exp_f32_e32 v150, v150
	v_exp_f32_e32 v151, v151
	v_add_f32_e32 v148, 1.0, v148
	v_add_f32_e32 v149, 1.0, v149
	v_add_f32_e32 v150, 1.0, v150
	v_add_f32_e32 v151, 1.0, v151
	v_rcp_f32_e32 v148, v148
	v_rcp_f32_e32 v149, v149
	v_rcp_f32_e32 v150, v150
	v_rcp_f32_e32 v151, v151
	v_mul_f32_e32 v144, v148, v144
	v_mul_f32_e32 v145, v149, v145
	v_mul_f32_e32 v146, v150, v146
	v_mul_f32_e32 v147, v151, v147
	v_cvt_pk_f16_f32 v158, v144, v145
	v_cvt_pk_f16_f32 v159, v146, v147
	ds_write_b64 v160, v[158:159] offset:39200
	v_mul_f32_e32 v144, v22, v30
	v_mul_f32_e32 v145, v23, v31
	v_mul_f32_e32 v146, v24, v32
	v_mul_f32_e32 v147, v25, v33
	v_mul_f32_e32 v148, 0xbfb8aa3b, v22
	v_mul_f32_e32 v149, 0xbfb8aa3b, v23
	v_mul_f32_e32 v150, 0xbfb8aa3b, v24
	v_mul_f32_e32 v151, 0xbfb8aa3b, v25
	v_exp_f32_e32 v148, v148
	v_exp_f32_e32 v149, v149
	v_exp_f32_e32 v150, v150
	v_exp_f32_e32 v151, v151
	v_add_f32_e32 v148, 1.0, v148
	v_add_f32_e32 v149, 1.0, v149
	v_add_f32_e32 v150, 1.0, v150
	v_add_f32_e32 v151, 1.0, v151
	v_rcp_f32_e32 v148, v148
	v_rcp_f32_e32 v149, v149
	v_rcp_f32_e32 v150, v150
	v_rcp_f32_e32 v151, v151
	v_mul_f32_e32 v144, v148, v144
	v_mul_f32_e32 v145, v149, v145
	v_mul_f32_e32 v146, v150, v146
	v_mul_f32_e32 v147, v151, v147
	v_cvt_pk_f16_f32 v152, v144, v145
	v_cvt_pk_f16_f32 v153, v146, v147
	ds_write_b64 v160, v[152:153] offset:43520
	v_mul_f32_e32 v144, v18, v26
	v_mul_f32_e32 v145, v19, v27
	v_mul_f32_e32 v146, v20, v28
	v_mul_f32_e32 v147, v21, v29
	v_mul_f32_e32 v148, 0xbfb8aa3b, v18
	v_mul_f32_e32 v149, 0xbfb8aa3b, v19
	v_mul_f32_e32 v150, 0xbfb8aa3b, v20
	v_mul_f32_e32 v151, 0xbfb8aa3b, v21
	v_exp_f32_e32 v148, v148
	v_exp_f32_e32 v149, v149
	v_exp_f32_e32 v150, v150
	v_exp_f32_e32 v151, v151
	v_add_f32_e32 v148, 1.0, v148
	v_add_f32_e32 v149, 1.0, v149
	v_add_f32_e32 v150, 1.0, v150
	v_add_f32_e32 v151, 1.0, v151
	v_rcp_f32_e32 v148, v148
	v_rcp_f32_e32 v149, v149
	v_rcp_f32_e32 v150, v150
	v_rcp_f32_e32 v151, v151
	v_mul_f32_e32 v144, v148, v144
	v_mul_f32_e32 v145, v149, v145
	v_mul_f32_e32 v146, v150, v146
	v_mul_f32_e32 v147, v151, v147
	v_cvt_pk_f16_f32 v154, v144, v145
	v_cvt_pk_f16_f32 v155, v146, v147
	ds_write_b64 v160, v[154:155] offset:43552
	v_mul_f32_e32 v144, v6, v14
	v_mul_f32_e32 v145, v7, v15
	v_mul_f32_e32 v146, v8, v16
	v_mul_f32_e32 v147, v9, v17
	v_mul_f32_e32 v148, 0xbfb8aa3b, v6
	v_mul_f32_e32 v149, 0xbfb8aa3b, v7
	v_mul_f32_e32 v150, 0xbfb8aa3b, v8
	v_mul_f32_e32 v151, 0xbfb8aa3b, v9
	v_exp_f32_e32 v148, v148
	v_exp_f32_e32 v149, v149
	v_exp_f32_e32 v150, v150
	v_exp_f32_e32 v151, v151
	v_add_f32_e32 v148, 1.0, v148
	v_add_f32_e32 v149, 1.0, v149
	v_add_f32_e32 v150, 1.0, v150
	v_add_f32_e32 v151, 1.0, v151
	v_rcp_f32_e32 v148, v148
	v_rcp_f32_e32 v149, v149
	v_rcp_f32_e32 v150, v150
	v_rcp_f32_e32 v151, v151
	v_mul_f32_e32 v144, v148, v144
	v_mul_f32_e32 v145, v149, v145
	v_mul_f32_e32 v146, v150, v146
	v_mul_f32_e32 v147, v151, v147
	v_cvt_pk_f16_f32 v156, v144, v145
	v_cvt_pk_f16_f32 v157, v146, v147
	ds_write_b64 v160, v[156:157] offset:47872
	v_mul_f32_e32 v144, v2, v10
	v_mul_f32_e32 v145, v3, v11
	v_mul_f32_e32 v146, v4, v12
	v_mul_f32_e32 v147, v5, v13
	v_mul_f32_e32 v148, 0xbfb8aa3b, v2
	v_mul_f32_e32 v149, 0xbfb8aa3b, v3
	v_mul_f32_e32 v150, 0xbfb8aa3b, v4
	v_mul_f32_e32 v151, 0xbfb8aa3b, v5
	v_exp_f32_e32 v148, v148
	v_exp_f32_e32 v149, v149
	v_exp_f32_e32 v150, v150
	v_exp_f32_e32 v151, v151
	v_add_f32_e32 v148, 1.0, v148
	v_add_f32_e32 v149, 1.0, v149
	v_add_f32_e32 v150, 1.0, v150
	v_add_f32_e32 v151, 1.0, v151
	v_rcp_f32_e32 v148, v148
	v_rcp_f32_e32 v149, v149
	v_rcp_f32_e32 v150, v150
	v_rcp_f32_e32 v151, v151
	v_mul_f32_e32 v144, v148, v144
	v_mul_f32_e32 v145, v149, v145
	v_mul_f32_e32 v146, v150, v146
	v_mul_f32_e32 v147, v151, v147
	v_cvt_pk_f16_f32 v158, v144, v145
	v_cvt_pk_f16_f32 v159, v146, v147
	ds_write_b64 v160, v[158:159] offset:47904
	s_waitcnt lgkmcnt(0)
	s_barrier
	ds_read_b128 v[192:195], v161
	ds_read_b128 v[196:199], v161 offset:1088
	ds_read_b128 v[200:203], v161 offset:2176
	ds_read_b128 v[204:207], v161 offset:3264
	ds_read_b128 v[208:211], v161 offset:4352
	ds_read_b128 v[212:215], v161 offset:5440
	ds_read_b128 v[216:219], v161 offset:6528
	ds_read_b128 v[220:223], v161 offset:7616
	s_waitcnt lgkmcnt(7)
	v_mov_b32_e32 v165, v164
	buffer_store_dwordx4 v[192:195], v165, s[72:75], 0 offen sc1
	s_waitcnt lgkmcnt(6)
	v_add_u32_e32 v166, 0x2000, v164
	buffer_store_dwordx4 v[196:199], v166, s[72:75], 0 offen sc1
	s_waitcnt lgkmcnt(5)
	v_add_u32_e32 v167, 0x4000, v164
	buffer_store_dwordx4 v[200:203], v167, s[72:75], 0 offen sc1
	s_waitcnt lgkmcnt(4)
	v_add_u32_e32 v168, 0x6000, v164
	buffer_store_dwordx4 v[204:207], v168, s[72:75], 0 offen sc1
	s_waitcnt lgkmcnt(3)
	v_add_u32_e32 v165, 0x8000, v164
	buffer_store_dwordx4 v[208:211], v165, s[72:75], 0 offen sc1
	s_waitcnt lgkmcnt(2)
	v_add_u32_e32 v166, 0xa000, v164
	buffer_store_dwordx4 v[212:215], v166, s[72:75], 0 offen sc1
	s_waitcnt lgkmcnt(1)
	v_add_u32_e32 v167, 0xc000, v164
	buffer_store_dwordx4 v[216:219], v167, s[72:75], 0 offen sc1
	s_waitcnt lgkmcnt(0)
	v_add_u32_e32 v168, 0xe000, v164
	buffer_store_dwordx4 v[220:223], v168, s[72:75], 0 offen sc1
	s_waitcnt vmcnt(0)
	s_barrier
	s_and_saveexec_b64 s[4:5], s[2:3]
	s_cbranch_execz .LBB2_5
	s_mov_b64 s[10:11], exec
	v_mbcnt_lo_u32_b32 v2, s10, 0
	v_mbcnt_hi_u32_b32 v2, s11, v2
	v_cmp_eq_u32_e32 vcc, 0, v2
	s_and_saveexec_b64 s[2:3], vcc
	s_cbranch_execz .LBB2_390
	s_ashr_i32 s97, s96, 31
	s_lshl_b64 s[34:35], s[96:97], 2
	s_add_u32 s34, s8, s34
	s_addc_u32 s35, s9, s35
	s_bcnt1_i32_b64 s10, s[10:11]
	v_mov_b32_e32 v2, s10
	global_atomic_add v163, v2, s[34:35]

.Lg1p_loop:
	ds_read_b128 v[152:155], v151
	ds_read_b128 v[156:159], v151 offset:1024
	ds_read_b128 v[164:167], v151 offset:2048
	ds_read_b128 v[168:171], v151 offset:3072
	s_lshl_b32 s58, s84, 7
	s_add_u32 s59, s24, s58
	s_addc_u32 s91, s25, 0
	s_add_u32 s92, s59, 0x80
	s_addc_u32 s93, s91, 0
	s_add_i32 s56, s52, 0xc000
	s_mov_b32 m0, s56
	v_lshl_add_u64 v[160:161], s[92:93], 0, v[132:133]
	s_add_i32 s33, s52, 0xe000
	ds_read_b128 v[172:175], v147
	ds_read_b128 v[176:179], v147 offset:1024
	ds_read_b128 v[184:187], v146
	ds_read_b128 v[188:191], v146 offset:1024
	ds_read_b128 v[192:195], v145
	ds_read_b128 v[196:199], v145 offset:1024
	ds_read_b128 v[200:203], v144
	ds_read_b128 v[204:207], v144 offset:1024
	global_load_lds_dwordx4 v[160:161], off
	v_lshl_add_u64 v[160:161], s[92:93], 0, v[130:131]
	s_mov_b32 m0, s33
	s_nop 0
	global_load_lds_dwordx4 v[160:161], off
	s_waitcnt lgkmcnt(8)
	s_barrier
	s_setprio 1
	s_waitcnt lgkmcnt(0)
	s_bitcmp1_b32 s100, 0
	s_cbranch_scc1 .Lg1p_skip1
	v_mfma_f32_16x16x32_f16 v[126:129], v[152:155], v[172:175], v[126:129]
	v_mfma_f32_16x16x32_f16 v[122:125], v[164:167], v[172:175], v[122:125]
	v_mfma_f32_16x16x32_f16 v[118:121], v[152:155], v[184:187], v[118:121]
	v_mfma_f32_16x16x32_f16 v[114:117], v[164:167], v[184:187], v[114:117]
	v_mfma_f32_16x16x32_f16 v[110:113], v[152:155], v[192:195], v[110:113]
	v_mfma_f32_16x16x32_f16 v[106:109], v[164:167], v[192:195], v[106:109]
	v_mfma_f32_16x16x32_f16 v[102:105], v[152:155], v[200:203], v[102:105]
	v_mfma_f32_16x16x32_f16 v[98:101], v[164:167], v[200:203], v[98:101]
	v_mfma_f32_16x16x32_f16 v[126:129], v[156:159], v[176:179], v[126:129]
	v_mfma_f32_16x16x32_f16 v[122:125], v[168:171], v[176:179], v[122:125]
	v_mfma_f32_16x16x32_f16 v[118:121], v[156:159], v[188:191], v[118:121]
	v_mfma_f32_16x16x32_f16 v[114:117], v[168:171], v[188:191], v[114:117]
	v_mfma_f32_16x16x32_f16 v[110:113], v[156:159], v[196:199], v[110:113]
	v_mfma_f32_16x16x32_f16 v[106:109], v[168:171], v[196:199], v[106:109]
	v_mfma_f32_16x16x32_f16 v[102:105], v[156:159], v[204:207], v[102:105]
	v_mfma_f32_16x16x32_f16 v[98:101], v[168:171], v[204:207], v[98:101]
.Lg1p_skip1:
	s_setprio 0
	s_barrier
	s_add_i32 s57, s84, 2
	s_lshl_b32 s82, s57, 7
	s_add_u32 s92, s4, s82
	s_addc_u32 s93, s5, 0
	s_mov_b32 m0, s53
	v_lshl_add_u64 v[160:161], s[92:93], 0, v[162:163]
	s_add_u32 s92, s92, 0x40000
	s_addc_u32 s93, s93, 0
	ds_read_b128 v[208:211], v150
	ds_read_b128 v[212:215], v150 offset:1024
	ds_read_b128 v[216:219], v150 offset:2048
	ds_read_b128 v[220:223], v150 offset:3072
	global_load_lds_dwordx4 v[160:161], off
	s_mov_b32 m0, s55
	v_lshl_add_u64 v[160:161], s[92:93], 0, v[162:163]
	global_load_lds_dwordx4 v[160:161], off
	s_barrier
	s_setprio 1
	s_waitcnt lgkmcnt(0)
	s_bitcmp1_b32 s100, 0
	s_cbranch_scc1 .Lg1p_skip2
	v_mfma_f32_16x16x32_f16 v[94:97], v[208:211], v[172:175], v[94:97]
	v_mfma_f32_16x16x32_f16 v[90:93], v[216:219], v[172:175], v[90:93]
	v_mfma_f32_16x16x32_f16 v[86:89], v[208:211], v[184:187], v[86:89]
	v_mfma_f32_16x16x32_f16 v[82:85], v[216:219], v[184:187], v[82:85]
	v_mfma_f32_16x16x32_f16 v[78:81], v[208:211], v[192:195], v[78:81]
	v_mfma_f32_16x16x32_f16 v[74:77], v[216:219], v[192:195], v[74:77]
	v_mfma_f32_16x16x32_f16 v[70:73], v[208:211], v[200:203], v[70:73]
	v_mfma_f32_16x16x32_f16 v[66:69], v[216:219], v[200:203], v[66:69]
	v_mfma_f32_16x16x32_f16 v[94:97], v[212:215], v[176:179], v[94:97]
	v_mfma_f32_16x16x32_f16 v[90:93], v[220:223], v[176:179], v[90:93]
	v_mfma_f32_16x16x32_f16 v[86:89], v[212:215], v[188:191], v[86:89]
	v_mfma_f32_16x16x32_f16 v[82:85], v[220:223], v[188:191], v[82:85]
	v_mfma_f32_16x16x32_f16 v[78:81], v[212:215], v[196:199], v[78:81]
	v_mfma_f32_16x16x32_f16 v[74:77], v[220:223], v[196:199], v[74:77]
	v_mfma_f32_16x16x32_f16 v[70:73], v[212:215], v[204:207], v[70:73]
	v_mfma_f32_16x16x32_f16 v[66:69], v[220:223], v[204:207], v[66:69]
.Lg1p_skip2:
	s_setprio 0
	s_add_u32 s92, s24, s82
	s_addc_u32 s93, s25, 0
	s_mov_b32 m0, s52
	s_barrier
	v_lshl_add_u64 v[160:161], s[92:93], 0, v[134:135]
	ds_read_b128 v[172:175], v147 offset:16384
	ds_read_b128 v[176:179], v147 offset:17408
	ds_read_b128 v[184:187], v146 offset:16384
	ds_read_b128 v[188:191], v146 offset:17408
	ds_read_b128 v[192:195], v145 offset:16384
	ds_read_b128 v[196:199], v145 offset:17408
	ds_read_b128 v[200:203], v144 offset:16384
	ds_read_b128 v[204:207], v144 offset:17408
	global_load_lds_dwordx4 v[160:161], off
	v_lshl_add_u64 v[160:161], s[92:93], 0, v[136:137]
	s_mov_b32 m0, s86
	s_nop 0
	global_load_lds_dwordx4 v[160:161], off
	s_barrier
	s_setprio 1
	s_waitcnt lgkmcnt(0)
	s_bitcmp1_b32 s100, 1
	s_cbranch_scc1 .Lg1p_skip3
	v_mfma_f32_16x16x32_f16 v[62:65], v[152:155], v[172:175], v[62:65]
	v_mfma_f32_16x16x32_f16 v[58:61], v[164:167], v[172:175], v[58:61]
	v_mfma_f32_16x16x32_f16 v[54:57], v[152:155], v[184:187], v[54:57]
	v_mfma_f32_16x16x32_f16 v[50:53], v[164:167], v[184:187], v[50:53]
	v_mfma_f32_16x16x32_f16 v[46:49], v[152:155], v[192:195], v[46:49]
	v_mfma_f32_16x16x32_f16 v[42:45], v[164:167], v[192:195], v[42:45]
	v_mfma_f32_16x16x32_f16 v[38:41], v[152:155], v[200:203], v[38:41]
	v_mfma_f32_16x16x32_f16 v[34:37], v[164:167], v[200:203], v[34:37]
	v_mfma_f32_16x16x32_f16 v[62:65], v[156:159], v[176:179], v[62:65]
	v_mfma_f32_16x16x32_f16 v[58:61], v[168:171], v[176:179], v[58:61]
	v_mfma_f32_16x16x32_f16 v[54:57], v[156:159], v[188:191], v[54:57]
	v_mfma_f32_16x16x32_f16 v[50:53], v[168:171], v[188:191], v[50:53]
	v_mfma_f32_16x16x32_f16 v[46:49], v[156:159], v[196:199], v[46:49]
	v_mfma_f32_16x16x32_f16 v[42:45], v[168:171], v[196:199], v[42:45]
	v_mfma_f32_16x16x32_f16 v[38:41], v[156:159], v[204:207], v[38:41]
	v_mfma_f32_16x16x32_f16 v[34:37], v[168:171], v[204:207], v[34:37]
.Lg1p_skip3:
	s_setprio 0
	s_barrier
	s_add_u32 s94, s10, s82
	s_addc_u32 s95, s11, 0
	s_mov_b32 m0, s87
	v_lshl_add_u64 v[152:153], s[94:95], 0, v[162:163]
	s_add_u32 s94, s94, 0x40000
	s_addc_u32 s95, s95, 0
	global_load_lds_dwordx4 v[152:153], off
	s_mov_b32 m0, s88
	v_lshl_add_u64 v[152:153], s[94:95], 0, v[162:163]
	global_load_lds_dwordx4 v[152:153], off
	s_waitcnt vmcnt(6)
	s_barrier
	s_setprio 1
	s_bitcmp1_b32 s100, 1
	s_cbranch_scc1 .Lg1p_skip4
	v_mfma_f32_16x16x32_f16 v[30:33], v[208:211], v[172:175], v[30:33]
	v_mfma_f32_16x16x32_f16 v[26:29], v[216:219], v[172:175], v[26:29]
	v_mfma_f32_16x16x32_f16 v[22:25], v[208:211], v[184:187], v[22:25]
	v_mfma_f32_16x16x32_f16 v[18:21], v[216:219], v[184:187], v[18:21]
	v_mfma_f32_16x16x32_f16 v[14:17], v[208:211], v[192:195], v[14:17]
	v_mfma_f32_16x16x32_f16 v[10:13], v[216:219], v[192:195], v[10:13]
	v_mfma_f32_16x16x32_f16 v[6:9], v[208:211], v[200:203], v[6:9]
	v_mfma_f32_16x16x32_f16 v[2:5], v[216:219], v[200:203], v[2:5]
	v_mfma_f32_16x16x32_f16 v[30:33], v[212:215], v[176:179], v[30:33]
	v_mfma_f32_16x16x32_f16 v[26:29], v[220:223], v[176:179], v[26:29]
	v_mfma_f32_16x16x32_f16 v[22:25], v[212:215], v[188:191], v[22:25]
	v_mfma_f32_16x16x32_f16 v[18:21], v[220:223], v[188:191], v[18:21]
	v_mfma_f32_16x16x32_f16 v[14:17], v[212:215], v[196:199], v[14:17]
	v_mfma_f32_16x16x32_f16 v[10:13], v[220:223], v[196:199], v[10:13]
	v_mfma_f32_16x16x32_f16 v[6:9], v[212:215], v[204:207], v[6:9]
	v_mfma_f32_16x16x32_f16 v[2:5], v[220:223], v[204:207], v[2:5]
.Lg1p_skip4:
	s_setprio 0
	s_barrier
	ds_read_b128 v[152:155], v149
	ds_read_b128 v[156:159], v149 offset:1024
	ds_read_b128 v[164:167], v149 offset:2048
	ds_read_b128 v[168:171], v149 offset:3072
	s_mov_b32 m0, s89
	v_lshl_add_u64 v[160:161], s[92:93], 0, v[132:133]
	ds_read_b128 v[172:175], v147 offset:32768
	ds_read_b128 v[176:179], v147 offset:33792
	ds_read_b128 v[184:187], v146 offset:32768
	ds_read_b128 v[188:191], v146 offset:33792
	ds_read_b128 v[192:195], v145 offset:32768
	ds_read_b128 v[196:199], v145 offset:33792
	ds_read_b128 v[200:203], v144 offset:32768
	ds_read_b128 v[204:207], v144 offset:33792
	global_load_lds_dwordx4 v[160:161], off
	v_lshl_add_u64 v[160:161], s[92:93], 0, v[130:131]
	s_mov_b32 m0, s90
	s_nop 0
	global_load_lds_dwordx4 v[160:161], off
	s_waitcnt lgkmcnt(8)
	s_barrier
	s_setprio 1
	s_waitcnt lgkmcnt(0)
	s_bitcmp1_b32 s100, 0
	s_cbranch_scc1 .Lg1p_skip5
	v_mfma_f32_16x16x32_f16 v[126:129], v[152:155], v[172:175], v[126:129]
	v_mfma_f32_16x16x32_f16 v[122:125], v[164:167], v[172:175], v[122:125]
	v_mfma_f32_16x16x32_f16 v[118:121], v[152:155], v[184:187], v[118:121]
	v_mfma_f32_16x16x32_f16 v[114:117], v[164:167], v[184:187], v[114:117]
	v_mfma_f32_16x16x32_f16 v[110:113], v[152:155], v[192:195], v[110:113]
	v_mfma_f32_16x16x32_f16 v[106:109], v[164:167], v[192:195], v[106:109]
	v_mfma_f32_16x16x32_f16 v[102:105], v[152:155], v[200:203], v[102:105]
	v_mfma_f32_16x16x32_f16 v[98:101], v[164:167], v[200:203], v[98:101]
	v_mfma_f32_16x16x32_f16 v[126:129], v[156:159], v[176:179], v[126:129]
	v_mfma_f32_16x16x32_f16 v[122:125], v[168:171], v[176:179], v[122:125]
	v_mfma_f32_16x16x32_f16 v[118:121], v[156:159], v[188:191], v[118:121]
	v_mfma_f32_16x16x32_f16 v[114:117], v[168:171], v[188:191], v[114:117]
	v_mfma_f32_16x16x32_f16 v[110:113], v[156:159], v[196:199], v[110:113]
	v_mfma_f32_16x16x32_f16 v[106:109], v[168:171], v[196:199], v[106:109]
	v_mfma_f32_16x16x32_f16 v[102:105], v[156:159], v[204:207], v[102:105]
	v_mfma_f32_16x16x32_f16 v[98:101], v[168:171], v[204:207], v[98:101]
.Lg1p_skip5:
	s_setprio 0
	s_barrier
	s_add_u32 s82, s4, s58
	s_addc_u32 s83, s5, 0
	s_add_u32 s92, s82, 0x180
	s_addc_u32 s93, s83, 0
	s_add_i32 m0, s52, 0x18000
	v_lshl_add_u64 v[160:161], s[92:93], 0, v[162:163]
	s_add_u32 s92, s92, 0x40000
	s_addc_u32 s93, s93, 0
	ds_read_b128 v[208:211], v148
	ds_read_b128 v[212:215], v148 offset:1024
	ds_read_b128 v[216:219], v148 offset:2048
	ds_read_b128 v[220:223], v148 offset:3072
	global_load_lds_dwordx4 v[160:161], off
	s_add_i32 m0, s52, 0x1a000
	v_lshl_add_u64 v[160:161], s[92:93], 0, v[162:163]
	global_load_lds_dwordx4 v[160:161], off
	s_barrier
	s_setprio 1
	s_waitcnt lgkmcnt(0)
	s_bitcmp1_b32 s100, 0
	s_cbranch_scc1 .Lg1p_skip6
	v_mfma_f32_16x16x32_f16 v[94:97], v[208:211], v[172:175], v[94:97]
	v_mfma_f32_16x16x32_f16 v[90:93], v[216:219], v[172:175], v[90:93]
	v_mfma_f32_16x16x32_f16 v[86:89], v[208:211], v[184:187], v[86:89]
	v_mfma_f32_16x16x32_f16 v[82:85], v[216:219], v[184:187], v[82:85]
	v_mfma_f32_16x16x32_f16 v[78:81], v[208:211], v[192:195], v[78:81]
	v_mfma_f32_16x16x32_f16 v[74:77], v[216:219], v[192:195], v[74:77]
	v_mfma_f32_16x16x32_f16 v[70:73], v[208:211], v[200:203], v[70:73]
	v_mfma_f32_16x16x32_f16 v[66:69], v[216:219], v[200:203], v[66:69]
	v_mfma_f32_16x16x32_f16 v[94:97], v[212:215], v[176:179], v[94:97]
	v_mfma_f32_16x16x32_f16 v[90:93], v[220:223], v[176:179], v[90:93]
	v_mfma_f32_16x16x32_f16 v[86:89], v[212:215], v[188:191], v[86:89]
	v_mfma_f32_16x16x32_f16 v[82:85], v[220:223], v[188:191], v[82:85]
	v_mfma_f32_16x16x32_f16 v[78:81], v[212:215], v[196:199], v[78:81]
	v_mfma_f32_16x16x32_f16 v[74:77], v[220:223], v[196:199], v[74:77]
	v_mfma_f32_16x16x32_f16 v[70:73], v[212:215], v[204:207], v[70:73]
	v_mfma_f32_16x16x32_f16 v[66:69], v[220:223], v[204:207], v[66:69]
.Lg1p_skip6:
	s_setprio 0
	s_add_u32 s92, s59, 0x180
	s_addc_u32 s93, s91, 0
	s_mov_b32 m0, s34
	s_barrier
	v_lshl_add_u64 v[160:161], s[92:93], 0, v[134:135]
	ds_read_b128 v[172:175], v147 offset:49152
	ds_read_b128 v[176:179], v147 offset:50176
	ds_read_b128 v[184:187], v146 offset:49152
	ds_read_b128 v[188:191], v146 offset:50176
	ds_read_b128 v[192:195], v145 offset:49152
	ds_read_b128 v[196:199], v145 offset:50176
	ds_read_b128 v[200:203], v144 offset:49152
	ds_read_b128 v[204:207], v144 offset:50176
	global_load_lds_dwordx4 v[160:161], off
	v_lshl_add_u64 v[160:161], s[92:93], 0, v[136:137]
	s_mov_b32 m0, s35
	s_nop 0
	global_load_lds_dwordx4 v[160:161], off
	s_barrier
	s_setprio 1
	s_waitcnt lgkmcnt(0)
	s_bitcmp1_b32 s100, 1
	s_cbranch_scc1 .Lg1p_skip7
	v_mfma_f32_16x16x32_f16 v[62:65], v[152:155], v[172:175], v[62:65]
	v_mfma_f32_16x16x32_f16 v[58:61], v[164:167], v[172:175], v[58:61]
	v_mfma_f32_16x16x32_f16 v[54:57], v[152:155], v[184:187], v[54:57]
	v_mfma_f32_16x16x32_f16 v[50:53], v[164:167], v[184:187], v[50:53]
	v_mfma_f32_16x16x32_f16 v[46:49], v[152:155], v[192:195], v[46:49]
	v_mfma_f32_16x16x32_f16 v[42:45], v[164:167], v[192:195], v[42:45]
	v_mfma_f32_16x16x32_f16 v[38:41], v[152:155], v[200:203], v[38:41]
	v_mfma_f32_16x16x32_f16 v[34:37], v[164:167], v[200:203], v[34:37]
	v_mfma_f32_16x16x32_f16 v[62:65], v[156:159], v[176:179], v[62:65]
	v_mfma_f32_16x16x32_f16 v[58:61], v[168:171], v[176:179], v[58:61]
	v_mfma_f32_16x16x32_f16 v[54:57], v[156:159], v[188:191], v[54:57]
	v_mfma_f32_16x16x32_f16 v[50:53], v[168:171], v[188:191], v[50:53]
	v_mfma_f32_16x16x32_f16 v[46:49], v[156:159], v[196:199], v[46:49]
	v_mfma_f32_16x16x32_f16 v[42:45], v[168:171], v[196:199], v[42:45]
	v_mfma_f32_16x16x32_f16 v[38:41], v[156:159], v[204:207], v[38:41]
	v_mfma_f32_16x16x32_f16 v[34:37], v[168:171], v[204:207], v[34:37]
.Lg1p_skip7:
	s_setprio 0
	s_barrier
	s_add_u32 s58, s10, s58
	s_addc_u32 s59, s11, 0
	s_add_u32 s58, s58, 0x180
	s_addc_u32 s59, s59, 0
	s_add_i32 m0, s52, 0x1c000
	v_lshl_add_u64 v[152:153], s[58:59], 0, v[162:163]
	s_add_u32 s58, s58, 0x40000
	s_addc_u32 s59, s59, 0
	global_load_lds_dwordx4 v[152:153], off
	s_add_i32 m0, s52, 0x1e000
	v_lshl_add_u64 v[152:153], s[58:59], 0, v[162:163]
	global_load_lds_dwordx4 v[152:153], off
	s_waitcnt vmcnt(6)
	s_barrier
	s_setprio 1
	s_bitcmp1_b32 s100, 1
	s_cbranch_scc1 .Lg1p_skip8
	v_mfma_f32_16x16x32_f16 v[30:33], v[208:211], v[172:175], v[30:33]
	v_mfma_f32_16x16x32_f16 v[26:29], v[216:219], v[172:175], v[26:29]
	v_mfma_f32_16x16x32_f16 v[22:25], v[208:211], v[184:187], v[22:25]
	v_mfma_f32_16x16x32_f16 v[18:21], v[216:219], v[184:187], v[18:21]
	v_mfma_f32_16x16x32_f16 v[14:17], v[208:211], v[192:195], v[14:17]
	v_mfma_f32_16x16x32_f16 v[10:13], v[216:219], v[192:195], v[10:13]
	v_mfma_f32_16x16x32_f16 v[6:9], v[208:211], v[200:203], v[6:9]
	v_mfma_f32_16x16x32_f16 v[2:5], v[216:219], v[200:203], v[2:5]
	v_mfma_f32_16x16x32_f16 v[30:33], v[212:215], v[176:179], v[30:33]
	v_mfma_f32_16x16x32_f16 v[26:29], v[220:223], v[176:179], v[26:29]
	v_mfma_f32_16x16x32_f16 v[22:25], v[212:215], v[188:191], v[22:25]
	v_mfma_f32_16x16x32_f16 v[18:21], v[220:223], v[188:191], v[18:21]
	v_mfma_f32_16x16x32_f16 v[14:17], v[212:215], v[196:199], v[14:17]
	v_mfma_f32_16x16x32_f16 v[10:13], v[220:223], v[196:199], v[10:13]
	v_mfma_f32_16x16x32_f16 v[6:9], v[212:215], v[204:207], v[6:9]
	v_mfma_f32_16x16x32_f16 v[2:5], v[220:223], v[204:207], v[2:5]
.Lg1p_skip8:
	s_setprio 0
	s_cmp_lt_u32 s84, 28
	s_mov_b32 s84, s57
	s_barrier
	s_cbranch_scc1 .Lg1p_loop
	v_readlane_b32 s4, v244, 8
	v_readlane_b32 s5, v244, 9
	s_mov_b32 m0, s56
	ds_read_b128 v[134:137], v151
	ds_read_b128 v[152:155], v151 offset:1024
	ds_read_b128 v[156:159], v151 offset:2048
	ds_read_b128 v[164:167], v151 offset:3072
	ds_read_b128 v[168:171], v147
	ds_read_b128 v[172:175], v147 offset:1024
	ds_read_b128 v[176:179], v146
	ds_read_b128 v[184:187], v146 offset:1024
	ds_read_b128 v[188:191], v145
	ds_read_b128 v[192:195], v145 offset:1024
	ds_read_b128 v[196:199], v144
	ds_read_b128 v[200:203], v144 offset:1024
	v_lshl_add_u64 v[132:133], s[4:5], 0, v[132:133]
	global_load_lds_dwordx4 v[132:133], off
	v_lshl_add_u64 v[130:131], s[4:5], 0, v[130:131]
	s_mov_b32 m0, s33
	s_nop 0
	global_load_lds_dwordx4 v[130:131], off
	s_barrier
	s_setprio 1
	s_waitcnt lgkmcnt(0)
	s_bitcmp1_b32 s100, 0
	s_cbranch_scc1 .Lg1p_skip9
	v_mfma_f32_16x16x32_f16 v[126:129], v[134:137], v[168:171], v[126:129]
	v_mfma_f32_16x16x32_f16 v[122:125], v[156:159], v[168:171], v[122:125]
	v_mfma_f32_16x16x32_f16 v[110:113], v[134:137], v[188:191], v[110:113]
	v_mfma_f32_16x16x32_f16 v[106:109], v[156:159], v[188:191], v[106:109]
	v_mfma_f32_16x16x32_f16 v[126:129], v[152:155], v[172:175], v[126:129]
	v_mfma_f32_16x16x32_f16 v[122:125], v[164:167], v[172:175], v[122:125]
	v_mfma_f32_16x16x32_f16 v[118:121], v[134:137], v[176:179], v[118:121]
	v_mfma_f32_16x16x32_f16 v[114:117], v[156:159], v[176:179], v[114:117]
	v_mfma_f32_16x16x32_f16 v[110:113], v[152:155], v[192:195], v[110:113]
	v_mfma_f32_16x16x32_f16 v[106:109], v[164:167], v[192:195], v[106:109]
	v_mfma_f32_16x16x32_f16 v[102:105], v[134:137], v[196:199], v[102:105]
	v_mfma_f32_16x16x32_f16 v[98:101], v[156:159], v[196:199], v[98:101]
	v_mfma_f32_16x16x32_f16 v[130:133], v[152:155], v[184:187], v[118:121]
	v_mfma_f32_16x16x32_f16 v[204:207], v[164:167], v[184:187], v[114:117]
	v_mfma_f32_16x16x32_f16 v[208:211], v[152:155], v[200:203], v[102:105]
	v_mfma_f32_16x16x32_f16 v[212:215], v[164:167], v[200:203], v[98:101]
.Lg1p_skip9:
	s_setprio 0
	s_barrier
	s_nop 1
	ds_read_b128 v[98:101], v150
	ds_read_b128 v[102:105], v150 offset:1024
	ds_read_b128 v[114:117], v150 offset:2048
	ds_read_b128 v[118:121], v150 offset:3072
	s_barrier
	s_setprio 1
	s_waitcnt lgkmcnt(0)
	s_bitcmp1_b32 s100, 0
	s_cbranch_scc1 .Lg1p_skip10
	v_mfma_f32_16x16x32_f16 v[94:97], v[98:101], v[168:171], v[94:97]
	v_mfma_f32_16x16x32_f16 v[90:93], v[114:117], v[168:171], v[90:93]
	v_mfma_f32_16x16x32_f16 v[78:81], v[98:101], v[188:191], v[78:81]
	v_mfma_f32_16x16x32_f16 v[74:77], v[114:117], v[188:191], v[74:77]
	v_mfma_f32_16x16x32_f16 v[94:97], v[102:105], v[172:175], v[94:97]
	v_mfma_f32_16x16x32_f16 v[90:93], v[118:121], v[172:175], v[90:93]
	v_mfma_f32_16x16x32_f16 v[86:89], v[98:101], v[176:179], v[86:89]
	v_mfma_f32_16x16x32_f16 v[82:85], v[114:117], v[176:179], v[82:85]
	v_mfma_f32_16x16x32_f16 v[78:81], v[102:105], v[192:195], v[78:81]
	v_mfma_f32_16x16x32_f16 v[74:77], v[118:121], v[192:195], v[74:77]
	v_mfma_f32_16x16x32_f16 v[70:73], v[98:101], v[196:199], v[70:73]
	v_mfma_f32_16x16x32_f16 v[66:69], v[114:117], v[196:199], v[66:69]
	v_mfma_f32_16x16x32_f16 v[168:171], v[102:105], v[184:187], v[86:89]
	v_mfma_f32_16x16x32_f16 v[172:175], v[118:121], v[184:187], v[82:85]
	v_mfma_f32_16x16x32_f16 v[176:179], v[102:105], v[200:203], v[70:73]
	v_mfma_f32_16x16x32_f16 v[184:187], v[118:121], v[200:203], v[66:69]
.Lg1p_skip10:
	s_setprio 0
	s_barrier
	s_nop 1
	ds_read_b128 v[66:69], v147 offset:16384
	ds_read_b128 v[70:73], v147 offset:17408
	ds_read_b128 v[82:85], v146 offset:16384
	ds_read_b128 v[86:89], v146 offset:17408
	ds_read_b128 v[188:191], v145 offset:16384
	ds_read_b128 v[192:195], v145 offset:17408
	ds_read_b128 v[196:199], v144 offset:16384
	ds_read_b128 v[200:203], v144 offset:17408
	s_waitcnt vmcnt(4)
	s_barrier
	s_setprio 1
	s_waitcnt lgkmcnt(0)
	s_bitcmp1_b32 s100, 1
	s_cbranch_scc1 .Lg1p_skip11
	v_mfma_f32_16x16x32_f16 v[62:65], v[134:137], v[66:69], v[62:65]
	v_mfma_f32_16x16x32_f16 v[58:61], v[156:159], v[66:69], v[58:61]
	v_mfma_f32_16x16x32_f16 v[46:49], v[134:137], v[188:191], v[46:49]
	v_mfma_f32_16x16x32_f16 v[42:45], v[156:159], v[188:191], v[42:45]
	v_mfma_f32_16x16x32_f16 v[62:65], v[152:155], v[70:73], v[62:65]
	v_mfma_f32_16x16x32_f16 v[58:61], v[164:167], v[70:73], v[58:61]
	v_mfma_f32_16x16x32_f16 v[54:57], v[134:137], v[82:85], v[54:57]
	v_mfma_f32_16x16x32_f16 v[50:53], v[156:159], v[82:85], v[50:53]
	v_mfma_f32_16x16x32_f16 v[46:49], v[152:155], v[192:195], v[46:49]
	v_mfma_f32_16x16x32_f16 v[42:45], v[164:167], v[192:195], v[42:45]
	v_mfma_f32_16x16x32_f16 v[38:41], v[134:137], v[196:199], v[38:41]
	v_mfma_f32_16x16x32_f16 v[34:37], v[156:159], v[196:199], v[34:37]
	v_mfma_f32_16x16x32_f16 v[216:219], v[152:155], v[86:89], v[54:57]
	v_mfma_f32_16x16x32_f16 v[220:223], v[164:167], v[86:89], v[50:53]
	v_mfma_f32_16x16x32_f16 v[134:137], v[152:155], v[200:203], v[38:41]
	v_mfma_f32_16x16x32_f16 v[150:153], v[164:167], v[200:203], v[34:37]
.Lg1p_skip11:
	s_setprio 0
	s_setprio 1
	s_bitcmp1_b32 s100, 1
	s_cbranch_scc1 .Lg1p_skip12
	v_mfma_f32_16x16x32_f16 v[30:33], v[98:101], v[66:69], v[30:33]
	v_mfma_f32_16x16x32_f16 v[26:29], v[114:117], v[66:69], v[26:29]
	v_mfma_f32_16x16x32_f16 v[14:17], v[98:101], v[188:191], v[14:17]
	v_mfma_f32_16x16x32_f16 v[10:13], v[114:117], v[188:191], v[10:13]
	v_mfma_f32_16x16x32_f16 v[30:33], v[102:105], v[70:73], v[30:33]
	v_mfma_f32_16x16x32_f16 v[26:29], v[118:121], v[70:73], v[26:29]
	v_mfma_f32_16x16x32_f16 v[22:25], v[98:101], v[82:85], v[22:25]
	v_mfma_f32_16x16x32_f16 v[18:21], v[114:117], v[82:85], v[18:21]
	v_mfma_f32_16x16x32_f16 v[14:17], v[102:105], v[192:195], v[14:17]
	v_mfma_f32_16x16x32_f16 v[10:13], v[118:121], v[192:195], v[10:13]
	v_mfma_f32_16x16x32_f16 v[6:9], v[98:101], v[196:199], v[6:9]
	v_mfma_f32_16x16x32_f16 v[2:5], v[114:117], v[196:199], v[2:5]
	v_mfma_f32_16x16x32_f16 v[154:157], v[102:105], v[86:89], v[22:25]
	v_mfma_f32_16x16x32_f16 v[158:161], v[118:121], v[86:89], v[18:21]
	v_mfma_f32_16x16x32_f16 v[164:167], v[102:105], v[200:203], v[6:9]
	v_mfma_f32_16x16x32_f16 v[188:191], v[118:121], v[200:203], v[2:5]
.Lg1p_skip12:
	s_setprio 0
	s_barrier
	s_nop 1
	ds_read_b128 v[2:5], v149
	ds_read_b128 v[6:9], v149 offset:1024
	ds_read_b128 v[192:195], v149 offset:2048
	ds_read_b128 v[196:199], v149 offset:3072
	ds_read_b128 v[18:21], v147 offset:32768
	ds_read_b128 v[22:25], v147 offset:33792
	ds_read_b128 v[34:37], v146 offset:32768
	ds_read_b128 v[38:41], v146 offset:33792
	ds_read_b128 v[50:53], v145 offset:32768
	ds_read_b128 v[54:57], v145 offset:33792
	ds_read_b128 v[200:203], v144 offset:32768
	ds_read_b128 v[224:227], v144 offset:33792
	s_waitcnt vmcnt(2)
	s_barrier
	s_setprio 1
	s_waitcnt lgkmcnt(0)
	s_bitcmp1_b32 s100, 0
	s_cbranch_scc1 .Lg1p_skip13
	v_mfma_f32_16x16x32_f16 v[66:69], v[2:5], v[18:21], v[126:129]
	v_mfma_f32_16x16x32_f16 v[118:121], v[6:9], v[22:25], v[66:69]
	v_mfma_f32_16x16x32_f16 v[66:69], v[192:195], v[18:21], v[122:125]
	v_mfma_f32_16x16x32_f16 v[114:117], v[196:199], v[22:25], v[66:69]
	v_mfma_f32_16x16x32_f16 v[66:69], v[2:5], v[34:37], v[130:133]
	v_mfma_f32_16x16x32_f16 v[102:105], v[6:9], v[38:41], v[66:69]
	v_mfma_f32_16x16x32_f16 v[66:69], v[192:195], v[34:37], v[204:207]
	v_mfma_f32_16x16x32_f16 v[98:101], v[196:199], v[38:41], v[66:69]
	v_mfma_f32_16x16x32_f16 v[66:69], v[2:5], v[50:53], v[110:113]
	v_mfma_f32_16x16x32_f16 v[86:89], v[6:9], v[54:57], v[66:69]
	v_mfma_f32_16x16x32_f16 v[66:69], v[192:195], v[50:53], v[106:109]
	v_mfma_f32_16x16x32_f16 v[82:85], v[196:199], v[54:57], v[66:69]
	v_mfma_f32_16x16x32_f16 v[66:69], v[2:5], v[200:203], v[208:211]
	v_mfma_f32_16x16x32_f16 v[70:73], v[6:9], v[224:227], v[66:69]
	v_mfma_f32_16x16x32_f16 v[66:69], v[192:195], v[200:203], v[212:215]
	v_mfma_f32_16x16x32_f16 v[66:69], v[196:199], v[224:227], v[66:69]
.Lg1p_skip13:
	s_setprio 0
	s_barrier
	ds_read_b128 v[130:133], v148
	ds_read_b128 v[204:207], v148 offset:1024
	ds_read_b128 v[208:211], v148 offset:2048
	ds_read_b128 v[212:215], v148 offset:3072
	s_waitcnt vmcnt(0)
	s_barrier
	s_setprio 1
	s_waitcnt lgkmcnt(0)
	s_bitcmp1_b32 s100, 0
	s_cbranch_scc1 .Lg1p_skip14
	v_mfma_f32_16x16x32_f16 v[94:97], v[130:133], v[18:21], v[94:97]
	v_mfma_f32_16x16x32_f16 v[18:21], v[208:211], v[18:21], v[90:93]
	v_mfma_f32_16x16x32_f16 v[122:125], v[212:215], v[22:25], v[18:21]
	v_mfma_f32_16x16x32_f16 v[18:21], v[130:133], v[34:37], v[168:171]
	v_mfma_f32_16x16x32_f16 v[110:113], v[204:207], v[38:41], v[18:21]
	v_mfma_f32_16x16x32_f16 v[18:21], v[208:211], v[34:37], v[172:175]
	v_mfma_f32_16x16x32_f16 v[106:109], v[212:215], v[38:41], v[18:21]
	v_mfma_f32_16x16x32_f16 v[18:21], v[130:133], v[50:53], v[78:81]
	v_mfma_f32_16x16x32_f16 v[126:129], v[204:207], v[22:25], v[94:97]
	v_mfma_f32_16x16x32_f16 v[94:97], v[204:207], v[54:57], v[18:21]
	v_mfma_f32_16x16x32_f16 v[18:21], v[208:211], v[50:53], v[74:77]
	v_mfma_f32_16x16x32_f16 v[90:93], v[212:215], v[54:57], v[18:21]
	v_mfma_f32_16x16x32_f16 v[18:21], v[130:133], v[200:203], v[176:179]
	v_mfma_f32_16x16x32_f16 v[78:81], v[204:207], v[224:227], v[18:21]
	v_mfma_f32_16x16x32_f16 v[18:21], v[208:211], v[200:203], v[184:187]
	v_mfma_f32_16x16x32_f16 v[74:77], v[212:215], v[224:227], v[18:21]
.Lg1p_skip14:
	s_setprio 0
	s_barrier
	ds_read_b128 v[168:171], v147 offset:49152
	ds_read_b128 v[172:175], v147 offset:50176
	ds_read_b128 v[176:179], v146 offset:49152
	ds_read_b128 v[146:149], v146 offset:50176
	ds_read_b128 v[184:187], v145 offset:49152
	ds_read_b128 v[200:203], v145 offset:50176
	ds_read_b128 v[224:227], v144 offset:49152
	ds_read_b128 v[228:231], v144 offset:50176
	s_barrier
	s_setprio 1
	s_waitcnt lgkmcnt(0)
	s_bitcmp1_b32 s100, 1
	s_cbranch_scc1 .Lg1p_skip15
	v_mfma_f32_16x16x32_f16 v[18:21], v[2:5], v[168:171], v[62:65]
	v_mfma_f32_16x16x32_f16 v[54:57], v[6:9], v[172:175], v[18:21]
	v_mfma_f32_16x16x32_f16 v[18:21], v[192:195], v[168:171], v[58:61]
	v_mfma_f32_16x16x32_f16 v[50:53], v[196:199], v[172:175], v[18:21]
	v_mfma_f32_16x16x32_f16 v[18:21], v[2:5], v[176:179], v[216:219]
	v_mfma_f32_16x16x32_f16 v[38:41], v[6:9], v[146:149], v[18:21]
	v_mfma_f32_16x16x32_f16 v[18:21], v[192:195], v[176:179], v[220:223]
	v_mfma_f32_16x16x32_f16 v[34:37], v[196:199], v[146:149], v[18:21]
	v_mfma_f32_16x16x32_f16 v[18:21], v[2:5], v[184:187], v[46:49]
	v_mfma_f32_16x16x32_f16 v[2:5], v[2:5], v[224:227], v[134:137]
	v_mfma_f32_16x16x32_f16 v[22:25], v[6:9], v[200:203], v[18:21]
	v_mfma_f32_16x16x32_f16 v[18:21], v[192:195], v[184:187], v[42:45]
	v_mfma_f32_16x16x32_f16 v[6:9], v[6:9], v[228:231], v[2:5]
	v_mfma_f32_16x16x32_f16 v[2:5], v[192:195], v[224:227], v[150:153]
	v_mfma_f32_16x16x32_f16 v[18:21], v[196:199], v[200:203], v[18:21]
	v_mfma_f32_16x16x32_f16 v[2:5], v[196:199], v[228:231], v[2:5]
.Lg1p_skip15:
	s_setprio 0
	s_setprio 1
	s_bitcmp1_b32 s100, 1
	s_cbranch_scc1 .Lg1p_skip16
	v_mfma_f32_16x16x32_f16 v[26:29], v[208:211], v[168:171], v[26:29]
	v_mfma_f32_16x16x32_f16 v[58:61], v[212:215], v[172:175], v[26:29]
	v_mfma_f32_16x16x32_f16 v[26:29], v[130:133], v[176:179], v[154:157]
	v_mfma_f32_16x16x32_f16 v[46:49], v[204:207], v[146:149], v[26:29]
	v_mfma_f32_16x16x32_f16 v[26:29], v[208:211], v[176:179], v[158:161]
	v_mfma_f32_16x16x32_f16 v[10:13], v[208:211], v[184:187], v[10:13]
	v_mfma_f32_16x16x32_f16 v[30:33], v[130:133], v[168:171], v[30:33]
	v_mfma_f32_16x16x32_f16 v[42:45], v[212:215], v[146:149], v[26:29]
	v_mfma_f32_16x16x32_f16 v[14:17], v[130:133], v[184:187], v[14:17]
	v_mfma_f32_16x16x32_f16 v[26:29], v[212:215], v[200:203], v[10:13]
	v_mfma_f32_16x16x32_f16 v[10:13], v[130:133], v[224:227], v[164:167]
	v_mfma_f32_16x16x32_f16 v[62:65], v[204:207], v[172:175], v[30:33]
	v_mfma_f32_16x16x32_f16 v[30:33], v[204:207], v[200:203], v[14:17]
	v_mfma_f32_16x16x32_f16 v[14:17], v[204:207], v[228:231], v[10:13]
	v_mfma_f32_16x16x32_f16 v[10:13], v[208:211], v[224:227], v[188:191]
	v_mfma_f32_16x16x32_f16 v[10:13], v[212:215], v[228:231], v[10:13]
